# deferred weight-conversion split: 2800 gate/up + 1290 down tiles deferred, idle-slot quotas 8/10/9/10
# baseline (speedup 1.0000x reference)
; __device__ __forceinline__ void bt_load(const float* __restrict__ src, int N, int perm, int it, int ntn, f32x4 (&v)[8]) {
;     const int wid = threadIdx.x >> 6, lane = threadIdx.x & 63;
;     const int per = 16 * ntn, z = it / per, r = it % per, kt = r / ntn, nt = r % ntn;
;     const int np = nt * 256 + lane * 4;
;     const int sc = perm ? (nt * 128 + (lane & 31) * 4 + (lane >> 5) * 1024) : np;
;     const float* p = src + (size_t)z * 1024 * N + (size_t)(kt * 64 + wid * 8) * N + sc;
; #pragma unroll
;     for (int i = 0; i < 8; ++i) v[i] = __builtin_nontemporal_load((const f32x4*)(p + (size_t)i * N));
; __device__ __forceinline__ void ph_big_transpose(const float* __restrict__ src, int N, int perm, int batch, bf16* __restrict__ dst, float* tile  , int G, int ndefer) {
;     const int tid = threadIdx.x, wid = tid >> 6, lane = tid & 63, ntn = N / 256, total = batch * 16 * ntn - ndefer;
;     int it = (int)blockIdx.x;
;     if (it >= total) return;
;     f32x4 cur[8], nxt[8], nx2[8];
;     bt_load(src, N, perm, it, ntn, cur);
;     if (it + G < total) bt_load(src, N, perm, it + G, ntn, nxt);
;     for (; it < total; it += G) {
;         const bool more = it + G < total, more2 = it + 2 * G < total;
;         if (more2) bt_load(src, N, perm, it + 2 * G, ntn, nx2);
.LBB0_63:
	s_cmpk_gt_i32 s2, 0x150f
	s_waitcnt lgkmcnt(0)
	s_barrier
	s_cbranch_scc1 .LBB0_71
	s_ashr_i32 s0, s2, 31
	s_lshr_b32 s0, s0, 25
	s_add_i32 s1, s2, s0
	s_ashr_i32 s0, s1, 7
	s_and_b32 s1, s1, 0xff80
	s_sub_i32 s1, s2, s1
	s_bfe_i32 s4, s1, 0x80000
	s_bfe_u32 s4, s4, 0x3000c
	s_add_i32 s4, s1, s4
	s_bfe_i32 s5, s4, 0x80000
	s_and_b32 s4, s4, 0xf8
	v_lshlrev_b32_e32 v2, 2, v0
	s_sub_i32 s1, s1, s4
	v_and_b32_e32 v2, 0x7c, v2
	v_lshlrev_b32_e32 v3, 5, v0
	s_movk_i32 s4, 0x400
	s_sext_i32_i8 s1, s1
	v_and_or_b32 v99, v3, s4, v2
	v_lshl_add_u32 v2, s1, 7, v99
	s_ashr_i32 s1, s0, 31
	s_lshl_b64 s[0:1], s[0:1], 23
	s_sext_i32_i16 s5, s5
	s_add_u32 s0, s68, s0
	s_addc_u32 s1, s69, s1
	s_lshl_b32 s4, s5, 3
	v_lshrrev_b32_e32 v3, 3, v0
	s_andn2_b32 s4, s4, 63
	v_and_b32_e32 v110, 56, v3
	v_or_b32_e32 v4, s4, v110
	v_ashrrev_i32_e32 v5, 31, v4
	v_lshlrev_b64 v[4:5], 13, v[4:5]
	v_lshl_add_u64 v[4:5], s[0:1], 0, v[4:5]
	v_ashrrev_i32_e32 v3, 31, v2
	v_lshl_add_u64 v[2:3], v[2:3], 2, v[4:5]
	s_movk_i32 s0, 0x2000
	v_add_co_u32_e32 v4, vcc, s0, v2
	s_movk_i32 s1, 0x4000
	s_nop 0
	v_addc_co_u32_e32 v5, vcc, 0, v3, vcc
	global_load_dwordx4 v[38:41], v[2:3], off nt
	global_load_dwordx4 v[34:37], v[4:5], off nt
	v_add_co_u32_e32 v4, vcc, s1, v2
	s_movk_i32 s4, 0x6000
	s_nop 0
	v_addc_co_u32_e32 v5, vcc, 0, v3, vcc
	v_add_co_u32_e32 v6, vcc, s4, v2
	s_mov_b32 s5, 0x8000
	s_nop 0
	v_addc_co_u32_e32 v7, vcc, 0, v3, vcc
	global_load_dwordx4 v[46:49], v[4:5], off nt
	global_load_dwordx4 v[42:45], v[6:7], off nt
	v_add_co_u32_e32 v4, vcc, s5, v2
	s_mov_b32 s6, 0xa000
	s_nop 0
	v_addc_co_u32_e32 v5, vcc, 0, v3, vcc
	v_add_co_u32_e32 v6, vcc, s6, v2
	s_add_i32 s6, s62, s2
	s_nop 0
	v_addc_co_u32_e32 v7, vcc, 0, v3, vcc
	global_load_dwordx4 v[54:57], v[4:5], off nt
	global_load_dwordx4 v[50:53], v[6:7], off nt
	v_add_co_u32_e32 v4, vcc, 0xc000, v2
	s_cmpk_gt_i32 s6, 0x150f
	s_nop 0
	v_addc_co_u32_e32 v5, vcc, 0, v3, vcc
	v_add_co_u32_e32 v2, vcc, 0xe000, v2
	s_nop 1
	v_addc_co_u32_e32 v3, vcc, 0, v3, vcc
	global_load_dwordx4 v[62:65], v[4:5], off nt
	global_load_dwordx4 v[58:61], v[2:3], off nt
	s_cbranch_scc1 .LBB0_66
	s_ashr_i32 s7, s6, 31
	s_lshr_b32 s7, s7, 25
	s_add_i32 s7, s6, s7
	s_ashr_i32 s8, s7, 7
	s_and_b32 s7, s7, 0xff80
	s_sub_i32 s6, s6, s7
	s_bfe_i32 s7, s6, 0x80000
	s_bfe_u32 s7, s7, 0x3000c
	s_add_i32 s7, s6, s7
	s_bfe_i32 s9, s7, 0x80000
	s_and_b32 s7, s7, 0xf8
	s_sub_i32 s6, s6, s7
	s_sext_i32_i16 s10, s9
	s_sext_i32_i8 s6, s6
	s_ashr_i32 s9, s8, 31
	v_lshl_add_u32 v2, s6, 7, v99
	s_lshl_b64 s[6:7], s[8:9], 23
	s_add_u32 s6, s68, s6
	s_addc_u32 s7, s69, s7
	s_lshl_b32 s8, s10, 3
	s_andn2_b32 s8, s8, 63
	v_or_b32_e32 v4, s8, v110
	v_ashrrev_i32_e32 v5, 31, v4
	v_lshlrev_b64 v[4:5], 13, v[4:5]
	v_lshl_add_u64 v[4:5], s[6:7], 0, v[4:5]
	v_ashrrev_i32_e32 v3, 31, v2
	v_lshl_add_u64 v[26:27], v[2:3], 2, v[4:5]
	v_add_co_u32_e32 v6, vcc, s0, v26
	s_nop 1
	v_addc_co_u32_e32 v7, vcc, 0, v27, vcc
	v_add_co_u32_e32 v10, vcc, s1, v26
	global_load_dwordx4 v[2:5], v[26:27], off nt
	s_nop 0
	global_load_dwordx4 v[6:9], v[6:7], off nt
	v_addc_co_u32_e32 v11, vcc, 0, v27, vcc
	v_add_co_u32_e32 v14, vcc, s4, v26
	s_nop 1
	v_addc_co_u32_e32 v15, vcc, 0, v27, vcc
	v_add_co_u32_e32 v18, vcc, s5, v26
	global_load_dwordx4 v[10:13], v[10:11], off nt
	s_nop 0
	global_load_dwordx4 v[14:17], v[14:15], off nt
	v_addc_co_u32_e32 v19, vcc, 0, v27, vcc
	v_add_co_u32_e32 v22, vcc, 0xa000, v26
	s_nop 1
	v_addc_co_u32_e32 v23, vcc, 0, v27, vcc
	v_add_co_u32_e32 v28, vcc, 0xc000, v26
	global_load_dwordx4 v[18:21], v[18:19], off nt
	s_nop 0
	global_load_dwordx4 v[22:25], v[22:23], off nt
	v_addc_co_u32_e32 v29, vcc, 0, v27, vcc
	v_add_co_u32_e32 v30, vcc, 0xe000, v26
	s_nop 1
	v_addc_co_u32_e32 v31, vcc, 0, v27, vcc
	global_load_dwordx4 v[26:29], v[28:29], off nt
	s_nop 0
	global_load_dwordx4 v[30:33], v[30:31], off nt

; __device__ __forceinline__ unsigned g8_cvt_pk(float lo, float hi) { unsigned r; asm volatile("v_cvt_pk_bf16_f32 %0, %1, %2" : "=v"(r) : "v"(lo), "v"(hi)); return r; }
; __device__ __forceinline__ void ph_big_transpose(const float* __restrict__ src, int N, int perm, int batch, bf16* __restrict__ dst, float* tile  , int G, int ndefer) {
;     ...
;     for (; it < total; it += G) {
;         const bool more = it + G < total, more2 = it + 2 * G < total;
;         if (more2) bt_load(src, N, perm, it + 2 * G, ntn, nx2);
;         __syncthreads();
; #pragma unroll
;         for (int i = 0; i < 8; ++i) { float* t = tile + (wid * 8 + i) * 257 + lane * 4; t[0] = cur[i][0]; t[1] = cur[i][1]; t[2] = cur[i][2]; t[3] = cur[i][3]; }
;         __syncthreads();
;         const int per = 16 * ntn, z = it / per, r = it % per, kt = r / ntn, nt = r % ntn;
;         bf16* d = dst + (size_t)z * N * 1024 + (((size_t)nt * 16 + kt) << 14);
;         const int kc = lane & 7;
; #pragma unroll
;         for (int pss = 0; pss < 4; ++pss) {
;             const int n = wid * 32 + pss * 8 + (lane >> 3); float f[8];
; #pragma unroll
;             for (int j = 0; j < 8; ++j) f[j] = tile[(kc * 8 + j) * 257 + n];
;             u32x4 w; w.x = g8_cvt_pk(f[0], f[1]); w.y = g8_cvt_pk(f[2], f[3]); w.z = g8_cvt_pk(f[4], f[5]); w.w = g8_cvt_pk(f[6], f[7]);
;             __builtin_nontemporal_store(w, (u32x4*)(d + n * 64 + kc * 8));
;         }
;         if (more) {
; #pragma unroll
;             for (int i = 0; i < 8; ++i) { cur[i] = nxt[i]; nxt[i] = nx2[i]; } }
;     }
.LBB0_67:
	s_barrier
	s_waitcnt vmcnt(7)
	ds_write_b128 v111, v[38:41]
	v_add_u32_e32 v38, 0x404, v111
	s_ashr_i32 s9, s8, 31
	s_waitcnt vmcnt(6)
	ds_write2_b32 v38, v34, v35 offset1:1
	v_add_u32_e32 v34, 0x40c, v111
	s_lshr_b32 s9, s9, 25
	ds_write2_b32 v34, v36, v37 offset1:1
	v_add_u32_e32 v34, 0x808, v111
	s_add_i32 s9, s8, s9
	s_waitcnt vmcnt(5)
	ds_write2_b64 v34, v[46:47], v[48:49] offset1:1
	v_add_u32_e32 v34, 0xc0c, v111
	s_ashr_i32 s10, s9, 7
	s_and_b32 s9, s9, 0xff80
	s_waitcnt vmcnt(4)
	ds_write2_b32 v34, v42, v43 offset1:1
	v_add_u32_e32 v34, 0xc14, v111
	s_sub_i32 s9, s8, s9
	s_add_i32 s31, s8, s62
	ds_write2_b32 v34, v44, v45 offset1:1
	s_waitcnt vmcnt(3)
	ds_write_b128 v111, v[54:57] offset:4112
	v_add_u32_e32 v34, 0x1414, v111
	s_bfe_i32 s8, s9, 0x80000
	s_waitcnt vmcnt(2)
	ds_write2_b32 v34, v50, v51 offset1:1
	v_add_u32_e32 v34, 0x141c, v111
	s_bfe_u32 s8, s8, 0x3000c
	ds_write2_b32 v34, v52, v53 offset1:1
	v_add_u32_e32 v34, 0x1818, v111
	s_add_i32 s11, s9, s8
	s_waitcnt vmcnt(1)
	ds_write2_b64 v34, v[62:63], v[64:65] offset1:1
	v_add_u32_e32 v34, 0x1c1c, v111
	s_bfe_i32 s8, s11, 0x80000
	s_and_b32 s11, s11, 0xf8
	s_waitcnt vmcnt(0)
	ds_write2_b32 v34, v58, v59 offset1:1
	v_add_u32_e32 v34, 0x1c24, v111
	s_sext_i32_i16 s8, s8
	s_sub_i32 s30, s9, s11
	s_ashr_i32 s11, s10, 31
	ds_write2_b32 v34, v60, v61 offset1:1
	s_waitcnt lgkmcnt(0)
	s_barrier
	s_lshr_b32 s8, s8, 3
	s_lshl_b64 s[10:11], s[10:11], 22
	ds_read_b32 v34, v112 offset:1028
	ds_read_b32 v35, v112 offset:3084
	ds_read_b32 v36, v112 offset:5140
	ds_read_b32 v37, v112 offset:7196
	ds_read_b32 v38, v112 offset:6168
	ds_read_b32 v39, v112 offset:4112
	ds_read_b32 v40, v112 offset:2056
	ds_read_b32 v41, v112
	s_add_u32 s33, s5, s10
	s_addc_u32 s34, s6, s11
	s_bfe_i64 s[10:11], s[30:31], 0x80000
	s_bfe_i64 s[8:9], s[8:9], 0x100000
	s_lshl_b64 s[10:11], s[10:11], 19
	s_add_u32 s10, s33, s10
	s_addc_u32 s11, s34, s11
	s_lshl_b64 s[8:9], s[8:9], 15
	s_waitcnt lgkmcnt(0)
	v_cvt_pk_bf16_f32 v34, v41, v34
	v_cvt_pk_bf16_f32 v35, v40, v35
	v_cvt_pk_bf16_f32 v36, v39, v36
	v_cvt_pk_bf16_f32 v37, v38, v37
	ds_read_b32 v42, v112 offset:1060
	ds_read_b32 v43, v112 offset:3116
	ds_read_b32 v44, v112 offset:5172
	ds_read_b32 v45, v112 offset:7228
	ds_read_b32 v46, v112 offset:6200
	ds_read_b32 v47, v112 offset:4144
	ds_read_b32 v48, v112 offset:2088
	ds_read_b32 v49, v112 offset:32
	s_add_u32 s8, s10, s8
	s_addc_u32 s9, s11, s9
	v_lshl_add_u64 v[38:39], s[8:9], 0, v[100:101]
	v_mov_b32_e32 v103, v101
	v_lshl_add_u64 v[40:41], v[38:39], 0, v[102:103]
	global_store_dwordx4 v[40:41], v[34:37], off nt
	v_mov_b32_e32 v105, v101
	v_lshl_add_u64 v[40:41], v[38:39], 0, v[104:105]
	s_waitcnt lgkmcnt(0)
	v_cvt_pk_bf16_f32 v34, v49, v42
	v_cvt_pk_bf16_f32 v35, v48, v43
	v_cvt_pk_bf16_f32 v36, v47, v44
	v_cvt_pk_bf16_f32 v37, v46, v45
	ds_read_b32 v42, v112 offset:1092
	ds_read_b32 v43, v112 offset:3148
	ds_read_b32 v44, v112 offset:5204
	ds_read_b32 v45, v112 offset:6232
	ds_read_b32 v46, v112 offset:4176
	ds_read_b32 v47, v112 offset:2120
	ds_read_b32 v48, v112 offset:64
	ds_read_b32 v49, v112 offset:7260
	global_store_dwordx4 v[40:41], v[34:37], off nt
	v_mov_b32_e32 v107, v101
	v_lshl_add_u64 v[40:41], v[38:39], 0, v[106:107]
	s_waitcnt lgkmcnt(1)
	v_cvt_pk_bf16_f32 v34, v48, v42
	v_cvt_pk_bf16_f32 v35, v47, v43
	v_cvt_pk_bf16_f32 v36, v46, v44
	s_waitcnt lgkmcnt(0)
	v_cvt_pk_bf16_f32 v37, v45, v49
	ds_read_b32 v42, v112 offset:1124
	ds_read_b32 v43, v112 offset:3180
	ds_read_b32 v44, v112 offset:5236
	ds_read_b32 v45, v112 offset:6264
	ds_read_b32 v46, v112 offset:4208
	ds_read_b32 v47, v112 offset:2152
	ds_read_b32 v48, v112 offset:96
	ds_read_b32 v49, v112 offset:7292
	v_mov_b32_e32 v109, v101
	global_store_dwordx4 v[40:41], v[34:37], off nt
	v_lshl_add_u64 v[38:39], v[38:39], 0, v[108:109]
	v_mov_b64_e32 v[60:61], v[32:33]
	s_waitcnt lgkmcnt(1)
	v_cvt_pk_bf16_f32 v34, v48, v42
	v_cvt_pk_bf16_f32 v35, v47, v43
	v_cvt_pk_bf16_f32 v36, v46, v44
	s_waitcnt lgkmcnt(0)
	v_cvt_pk_bf16_f32 v37, v45, v49
	global_store_dwordx4 v[38:39], v[34:37], off nt
	v_mov_b64_e32 v[64:65], v[28:29]
	v_mov_b64_e32 v[52:53], v[24:25]
	v_mov_b64_e32 v[56:57], v[20:21]
	v_mov_b64_e32 v[44:45], v[16:17]
	v_mov_b64_e32 v[48:49], v[12:13]
	v_mov_b64_e32 v[36:37], v[8:9]
	v_mov_b64_e32 v[40:41], v[4:5]
	v_mov_b64_e32 v[58:59], v[30:31]
	v_mov_b64_e32 v[62:63], v[26:27]
	v_mov_b64_e32 v[50:51], v[22:23]
	v_mov_b64_e32 v[54:55], v[18:19]
	v_mov_b64_e32 v[42:43], v[14:15]
	v_mov_b64_e32 v[46:47], v[10:11]
	v_mov_b64_e32 v[34:35], v[6:7]
	v_mov_b64_e32 v[38:39], v[2:3]
	v_mov_b64_e32 v[30:31], v[94:95]
	v_mov_b64_e32 v[26:27], v[90:91]
	v_mov_b64_e32 v[22:23], v[86:87]
	v_mov_b64_e32 v[18:19], v[82:83]
	v_mov_b64_e32 v[14:15], v[78:79]
	v_mov_b64_e32 v[10:11], v[74:75]
	v_mov_b64_e32 v[6:7], v[70:71]
	v_mov_b64_e32 v[2:3], v[66:67]
	s_cmpk_lt_i32 s31, 0x1510
	v_mov_b64_e32 v[32:33], v[96:97]
	v_mov_b64_e32 v[28:29], v[92:93]
	v_mov_b64_e32 v[24:25], v[88:89]
	v_mov_b64_e32 v[20:21], v[84:85]
	v_mov_b64_e32 v[16:17], v[80:81]
	v_mov_b64_e32 v[12:13], v[76:77]
	v_mov_b64_e32 v[8:9], v[72:73]
	v_mov_b64_e32 v[4:5], v[68:69]
	s_mov_b32 s8, s31
	s_cbranch_scc0 .LBB0_70
; __device__ __forceinline__ void bt_load(const float* __restrict__ src, int N, int perm, int it, int ntn, f32x4 (&v)[8]) {
;     const int wid = threadIdx.x >> 6, lane = threadIdx.x & 63;
;     const int per = 16 * ntn, z = it / per, r = it % per, kt = r / ntn, nt = r % ntn;
;     const int np = nt * 256 + lane * 4;
;     const int sc = perm ? (nt * 128 + (lane & 31) * 4 + (lane >> 5) * 1024) : np;
;     const float* p = src + (size_t)z * 1024 * N + (size_t)(kt * 64 + wid * 8) * N + sc;
; #pragma unroll
;     for (int i = 0; i < 8; ++i) v[i] = __builtin_nontemporal_load((const f32x4*)(p + (size_t)i * N));
; __device__ __forceinline__ void ph_big_transpose(const float* __restrict__ src, int N, int perm, int batch, bf16* __restrict__ dst, float* tile  , int G, int ndefer) {
;     ...
;     for (; it < total; it += G) {
;         const bool more = it + G < total, more2 = it + 2 * G < total;
;         if (more2) bt_load(src, N, perm, it + 2 * G, ntn, nx2);
.LBB0_68:
	s_add_i32 s9, s7, s8
	s_cmpk_gt_i32 s9, 0x150f
	s_cbranch_scc1 .LBB0_67
	s_ashr_i32 s10, s9, 31
	s_lshr_b32 s10, s10, 25
	s_add_i32 s11, s9, s10
	s_ashr_i32 s10, s11, 7
	s_and_b32 s11, s11, 0xff80
	s_sub_i32 s9, s9, s11
	s_bfe_i32 s11, s9, 0x80000
	s_bfe_u32 s11, s11, 0x3000c
	s_add_i32 s11, s9, s11
	s_bfe_i32 s30, s11, 0x80000
	s_and_b32 s11, s11, 0xf8
	s_sub_i32 s9, s9, s11
	s_ashr_i32 s11, s10, 31
	s_lshl_b64 s[10:11], s[10:11], 23
	s_sext_i32_i16 s30, s30
	s_sext_i32_i8 s9, s9
	s_add_u32 s10, s68, s10
	v_lshl_add_u32 v66, s9, 7, v99
	s_addc_u32 s11, s69, s11
	s_lshl_b32 s9, s30, 3
	s_andn2_b32 s9, s9, 63
	v_or_b32_e32 v68, s9, v110
	v_ashrrev_i32_e32 v69, 31, v68
	v_lshlrev_b64 v[68:69], 13, v[68:69]
	v_lshl_add_u64 v[68:69], s[10:11], 0, v[68:69]
	v_ashrrev_i32_e32 v67, 31, v66
	v_lshl_add_u64 v[90:91], v[66:67], 2, v[68:69]
	v_add_co_u32_e32 v70, vcc, s0, v90
	s_nop 1
	v_addc_co_u32_e32 v71, vcc, 0, v91, vcc
	v_add_co_u32_e32 v74, vcc, s1, v90
	global_load_dwordx4 v[66:69], v[90:91], off nt
	s_nop 0
	global_load_dwordx4 v[70:73], v[70:71], off nt
	v_addc_co_u32_e32 v75, vcc, 0, v91, vcc
	v_add_co_u32_e32 v78, vcc, s4, v90
	s_nop 1
	v_addc_co_u32_e32 v79, vcc, 0, v91, vcc
	v_add_co_u32_e32 v82, vcc, 0x8000, v90
	global_load_dwordx4 v[74:77], v[74:75], off nt
	s_nop 0
	global_load_dwordx4 v[78:81], v[78:79], off nt
	v_addc_co_u32_e32 v83, vcc, 0, v91, vcc
	v_add_co_u32_e32 v86, vcc, 0xa000, v90
	s_nop 1
	v_addc_co_u32_e32 v87, vcc, 0, v91, vcc
	v_add_co_u32_e32 v92, vcc, 0xc000, v90
	global_load_dwordx4 v[82:85], v[82:83], off nt
	s_nop 0
	global_load_dwordx4 v[86:89], v[86:87], off nt
	v_addc_co_u32_e32 v93, vcc, 0, v91, vcc
	v_add_co_u32_e32 v94, vcc, 0xe000, v90
	s_nop 1
	v_addc_co_u32_e32 v95, vcc, 0, v91, vcc
	global_load_dwordx4 v[90:93], v[92:93], off nt
	s_nop 0
	global_load_dwordx4 v[94:97], v[94:95], off nt
	s_branch .LBB0_67

; __device__ __forceinline__ void bt_load(const float* __restrict__ src, int N, int perm, int it, int ntn, f32x4 (&v)[8]) {
;     const int wid = threadIdx.x >> 6, lane = threadIdx.x & 63;
;     const int per = 16 * ntn, z = it / per, r = it % per, kt = r / ntn, nt = r % ntn;
;     const int np = nt * 256 + lane * 4;
;     const int sc = perm ? (nt * 128 + (lane & 31) * 4 + (lane >> 5) * 1024) : np;
;     const float* p = src + (size_t)z * 1024 * N + (size_t)(kt * 64 + wid * 8) * N + sc;
; #pragma unroll
;     for (int i = 0; i < 8; ++i) v[i] = __builtin_nontemporal_load((const f32x4*)(p + (size_t)i * N));
; __device__ __forceinline__ void ph_big_transpose(const float* __restrict__ src, int N, int perm, int batch, bf16* __restrict__ dst, float* tile  , int G, int ndefer) {
;     const int tid = threadIdx.x, wid = tid >> 6, lane = tid & 63, ntn = N / 256, total = batch * 16 * ntn - ndefer;
;     int it = (int)blockIdx.x;
;     if (it >= total) return;
;     f32x4 cur[8], nxt[8], nx2[8];
;     bt_load(src, N, perm, it, ntn, cur);
;     if (it + G < total) bt_load(src, N, perm, it + G, ntn, nxt);
;     for (; it < total; it += G) {
;         const bool more = it + G < total, more2 = it + 2 * G < total;
;         if (more2) bt_load(src, N, perm, it + 2 * G, ntn, nx2);
.LBB0_71:
	s_cmpk_gt_i32 s2, 0xaf5
	s_cbranch_scc1 .LBB0_79
	s_ashr_i32 s0, s2, 31
	s_lshr_b32 s0, s0, 26
	s_add_i32 s1, s2, s0
	s_ashr_i32 s0, s1, 6
	s_and_b32 s1, s1, 0xffc0
	s_sub_i32 s1, s2, s1
	s_bfe_i32 s4, s1, 0x80000
	s_bfe_u32 s4, s4, 0x2000d
	s_add_i32 s4, s1, s4
	s_bfe_i32 s5, s4, 0x80000
	s_and_b32 s4, s4, 0xfc
	s_sub_i32 s1, s1, s4
	v_lshlrev_b32_e32 v2, 2, v0
	s_sext_i32_i8 s1, s1
	v_and_b32_e32 v99, 0xfc, v2
	v_lshl_or_b32 v2, s1, 8, v99
	s_ashr_i32 s1, s0, 31
	s_lshl_b64 s[0:1], s[0:1], 22
	s_sext_i32_i16 s5, s5
	s_add_u32 s0, s72, s0
	s_addc_u32 s1, s73, s1
	s_lshl_b32 s4, s5, 4
	v_lshrrev_b32_e32 v3, 3, v0
	s_andn2_b32 s4, s4, 63
	v_and_b32_e32 v110, 56, v3
	v_or_b32_e32 v4, s4, v110
	v_ashrrev_i32_e32 v5, 31, v4
	v_lshlrev_b64 v[4:5], 12, v[4:5]
	v_lshl_add_u64 v[4:5], s[0:1], 0, v[4:5]
	v_ashrrev_i32_e32 v3, 31, v2
	v_lshl_add_u64 v[2:3], v[2:3], 2, v[4:5]
	s_movk_i32 s0, 0x2000
	v_add_co_u32_e32 v4, vcc, s0, v2
	s_movk_i32 s4, 0x4000
	s_nop 0
	v_addc_co_u32_e32 v5, vcc, 0, v3, vcc
	global_load_dwordx4 v[42:45], v[4:5], off offset:-4096 nt
	global_load_dwordx4 v[34:37], v[4:5], off nt
	v_add_co_u32_e32 v4, vcc, s4, v2
	s_movk_i32 s1, 0x5000
	s_nop 0
	v_addc_co_u32_e32 v5, vcc, 0, v3, vcc
	global_load_dwordx4 v[46:49], v[4:5], off offset:-4096 nt
	global_load_dwordx4 v[38:41], v[4:5], off nt
	v_add_co_u32_e32 v4, vcc, s1, v2
	s_add_i32 s5, s62, s2
	s_nop 0
	v_addc_co_u32_e32 v5, vcc, 0, v3, vcc
	global_load_dwordx4 v[62:65], v[2:3], off nt
	global_load_dwordx4 v[50:53], v[4:5], off nt
	v_add_co_u32_e32 v4, vcc, 0x6000, v2
	s_cmpk_gt_i32 s5, 0xaf5
	s_nop 0
	v_addc_co_u32_e32 v5, vcc, 0, v3, vcc
	v_add_co_u32_e32 v2, vcc, 0x7000, v2
	s_movk_i32 s1, 0x3000
	s_nop 0
	v_addc_co_u32_e32 v3, vcc, 0, v3, vcc
	global_load_dwordx4 v[58:61], v[4:5], off nt
	global_load_dwordx4 v[54:57], v[2:3], off nt
	s_cbranch_scc1 .LBB0_74
	s_ashr_i32 s6, s5, 31
	s_lshr_b32 s6, s6, 26
	s_add_i32 s7, s5, s6
	s_ashr_i32 s6, s7, 6
	s_and_b32 s7, s7, 0xffc0
	s_sub_i32 s5, s5, s7
	s_bfe_i32 s7, s5, 0x80000
	s_bfe_u32 s7, s7, 0x2000d
	s_add_i32 s7, s5, s7
	s_bfe_i32 s8, s7, 0x80000
	s_and_b32 s7, s7, 0xfc
	s_sub_i32 s5, s5, s7
	s_ashr_i32 s7, s6, 31
	s_lshl_b64 s[6:7], s[6:7], 22
	s_sext_i32_i16 s8, s8
	s_sext_i32_i8 s5, s5
	s_add_u32 s6, s72, s6
	v_lshl_or_b32 v2, s5, 8, v99
	s_addc_u32 s7, s73, s7
	s_lshl_b32 s5, s8, 4
	s_andn2_b32 s5, s5, 63
	v_or_b32_e32 v4, s5, v110
	v_ashrrev_i32_e32 v5, 31, v4
	v_lshlrev_b64 v[4:5], 12, v[4:5]
	v_lshl_add_u64 v[4:5], s[6:7], 0, v[4:5]
	v_ashrrev_i32_e32 v3, 31, v2
	v_lshl_add_u64 v[26:27], v[2:3], 2, v[4:5]
	v_add_co_u32_e32 v2, vcc, s0, v26
	s_nop 1
	v_addc_co_u32_e32 v3, vcc, 0, v27, vcc
	v_add_co_u32_e32 v10, vcc, s4, v26
	global_load_dwordx4 v[6:9], v[2:3], off offset:-4096 nt
	s_nop 0
	global_load_dwordx4 v[2:5], v[2:3], off nt
	v_addc_co_u32_e32 v11, vcc, 0, v27, vcc
	v_add_co_u32_e32 v18, vcc, 0x5000, v26
	global_load_dwordx4 v[14:17], v[10:11], off offset:-4096 nt
	s_nop 0
	global_load_dwordx4 v[10:13], v[10:11], off nt
	v_addc_co_u32_e32 v19, vcc, 0, v27, vcc
	v_add_co_u32_e32 v28, vcc, 0x6000, v26
	global_load_dwordx4 v[22:25], v[26:27], off nt
	s_nop 0
	global_load_dwordx4 v[18:21], v[18:19], off nt
	v_addc_co_u32_e32 v29, vcc, 0, v27, vcc
	v_add_co_u32_e32 v30, vcc, 0x7000, v26
	s_nop 1
	v_addc_co_u32_e32 v31, vcc, 0, v27, vcc
	global_load_dwordx4 v[26:29], v[28:29], off nt
	s_nop 0
	global_load_dwordx4 v[30:33], v[30:31], off nt

; __device__ __forceinline__ unsigned g8_cvt_pk(float lo, float hi) { unsigned r; asm volatile("v_cvt_pk_bf16_f32 %0, %1, %2" : "=v"(r) : "v"(lo), "v"(hi)); return r; }
; __device__ __forceinline__ void bt_load(const float* __restrict__ src, int N, int perm, int it, int ntn, f32x4 (&v)[8]) {
;     const int wid = threadIdx.x >> 6, lane = threadIdx.x & 63;
;     const int per = 16 * ntn, z = it / per, r = it % per, kt = r / ntn, nt = r % ntn;
;     const int np = nt * 256 + lane * 4;
;     const int sc = perm ? (nt * 128 + (lane & 31) * 4 + (lane >> 5) * 1024) : np;
;     const float* p = src + (size_t)z * 1024 * N + (size_t)(kt * 64 + wid * 8) * N + sc;
; #pragma unroll
;     for (int i = 0; i < 8; ++i) v[i] = __builtin_nontemporal_load((const f32x4*)(p + (size_t)i * N));
; __device__ __forceinline__ void ph_big_transpose(const float* __restrict__ src, int N, int perm, int batch, bf16* __restrict__ dst, float* tile  , int G, int ndefer) {
;     ...
;     for (; it < total; it += G) {
;         const bool more = it + G < total, more2 = it + 2 * G < total;
;         if (more2) bt_load(src, N, perm, it + 2 * G, ntn, nx2);
;         __syncthreads();
; #pragma unroll
;         for (int i = 0; i < 8; ++i) { float* t = tile + (wid * 8 + i) * 257 + lane * 4; t[0] = cur[i][0]; t[1] = cur[i][1]; t[2] = cur[i][2]; t[3] = cur[i][3]; }
;         __syncthreads();
;         const int per = 16 * ntn, z = it / per, r = it % per, kt = r / ntn, nt = r % ntn;
;         bf16* d = dst + (size_t)z * N * 1024 + (((size_t)nt * 16 + kt) << 14);
;         const int kc = lane & 7;
; #pragma unroll
;         for (int pss = 0; pss < 4; ++pss) {
;             const int n = wid * 32 + pss * 8 + (lane >> 3); float f[8];
; #pragma unroll
;             for (int j = 0; j < 8; ++j) f[j] = tile[(kc * 8 + j) * 257 + n];
;             u32x4 w; w.x = g8_cvt_pk(f[0], f[1]); w.y = g8_cvt_pk(f[2], f[3]); w.z = g8_cvt_pk(f[4], f[5]); w.w = g8_cvt_pk(f[6], f[7]);
;             __builtin_nontemporal_store(w, (u32x4*)(d + n * 64 + kc * 8));
;         }
;         if (more) {
; #pragma unroll
;             for (int i = 0; i < 8; ++i) { cur[i] = nxt[i]; nxt[i] = nx2[i]; } }
;     }
.LBB0_75:
	s_ashr_i32 s8, s3, 31
	s_barrier
	s_waitcnt vmcnt(3)
	ds_write_b128 v111, v[62:65]
	v_add_u32_e32 v62, 0x404, v111
	s_lshr_b32 s8, s8, 26
	ds_write2_b32 v62, v42, v43 offset1:1
	v_add_u32_e32 v42, 0x40c, v111
	s_add_i32 s9, s3, s8
	ds_write2_b32 v42, v44, v45 offset1:1
	v_add_u32_e32 v42, 0x808, v111
	s_ashr_i32 s8, s9, 6
	s_and_b32 s9, s9, 0xffc0
	s_add_i32 s7, s3, s62
	ds_write2_b64 v42, v[34:35], v[36:37] offset1:1
	v_add_u32_e32 v34, 0xc0c, v111
	s_sub_i32 s3, s3, s9
	ds_write2_b32 v34, v46, v47 offset1:1
	v_add_u32_e32 v34, 0xc14, v111
	s_bfe_i32 s9, s3, 0x80000
	ds_write2_b32 v34, v48, v49 offset1:1
	ds_write_b128 v111, v[38:41] offset:4112
	v_add_u32_e32 v34, 0x1414, v111
	s_bfe_u32 s9, s9, 0x2000d
	s_waitcnt vmcnt(2)
	ds_write2_b32 v34, v50, v51 offset1:1
	v_add_u32_e32 v34, 0x141c, v111
	s_add_i32 s9, s3, s9
	ds_write2_b32 v34, v52, v53 offset1:1
	v_add_u32_e32 v34, 0x1818, v111
	s_bfe_i32 s10, s9, 0x80000
	s_and_b32 s9, s9, 0xfc
	s_waitcnt vmcnt(1)
	ds_write2_b64 v34, v[58:59], v[60:61] offset1:1
	v_add_u32_e32 v34, 0x1c1c, v111
	s_sext_i32_i16 s10, s10
	s_sub_i32 s30, s3, s9
	s_ashr_i32 s9, s8, 31
	s_waitcnt vmcnt(0)
	ds_write2_b32 v34, v54, v55 offset1:1
	v_add_u32_e32 v34, 0x1c24, v111
	s_lshr_b32 s10, s10, 2
	s_lshl_b64 s[8:9], s[8:9], 21
	ds_write2_b32 v34, v56, v57 offset1:1
	s_waitcnt lgkmcnt(0)
	s_barrier
	s_add_u32 s3, s4, s8
	ds_read_b32 v34, v112 offset:1028
	ds_read_b32 v35, v112 offset:3084
	ds_read_b32 v36, v112 offset:5140
	ds_read_b32 v37, v112 offset:7196
	ds_read_b32 v38, v112 offset:6168
	ds_read_b32 v39, v112 offset:4112
	ds_read_b32 v40, v112 offset:2056
	ds_read_b32 v41, v112
	s_addc_u32 s31, s5, s9
	s_bfe_i64 s[8:9], s[30:31], 0x80000
	s_bfe_i64 s[10:11], s[10:11], 0x100000
	s_lshl_b64 s[8:9], s[8:9], 19
	s_add_u32 s3, s3, s8
	s_addc_u32 s30, s31, s9
	s_lshl_b64 s[8:9], s[10:11], 15
	s_waitcnt lgkmcnt(0)
	v_cvt_pk_bf16_f32 v34, v41, v34
	v_cvt_pk_bf16_f32 v35, v40, v35
	v_cvt_pk_bf16_f32 v36, v39, v36
	v_cvt_pk_bf16_f32 v37, v38, v37
	ds_read_b32 v42, v112 offset:1060
	ds_read_b32 v43, v112 offset:3116
	ds_read_b32 v44, v112 offset:5172
	ds_read_b32 v45, v112 offset:7228
	ds_read_b32 v46, v112 offset:6200
	ds_read_b32 v47, v112 offset:4144
	ds_read_b32 v48, v112 offset:2088
	ds_read_b32 v49, v112 offset:32
	s_add_u32 s8, s3, s8
	s_addc_u32 s9, s30, s9
	v_lshl_add_u64 v[38:39], s[8:9], 0, v[100:101]
	v_mov_b32_e32 v103, v101
	v_lshl_add_u64 v[40:41], v[38:39], 0, v[102:103]
	global_store_dwordx4 v[40:41], v[34:37], off nt
	v_mov_b32_e32 v105, v101
	v_lshl_add_u64 v[40:41], v[38:39], 0, v[104:105]
	s_waitcnt lgkmcnt(0)
	v_cvt_pk_bf16_f32 v34, v49, v42
	v_cvt_pk_bf16_f32 v35, v48, v43
	v_cvt_pk_bf16_f32 v36, v47, v44
	v_cvt_pk_bf16_f32 v37, v46, v45
	ds_read_b32 v42, v112 offset:1092
	ds_read_b32 v43, v112 offset:3148
	ds_read_b32 v44, v112 offset:5204
	ds_read_b32 v45, v112 offset:6232
	ds_read_b32 v46, v112 offset:4176
	ds_read_b32 v47, v112 offset:2120
	ds_read_b32 v48, v112 offset:64
	ds_read_b32 v49, v112 offset:7260
	global_store_dwordx4 v[40:41], v[34:37], off nt
	v_mov_b32_e32 v107, v101
	v_lshl_add_u64 v[40:41], v[38:39], 0, v[106:107]
	s_waitcnt lgkmcnt(1)
	v_cvt_pk_bf16_f32 v34, v48, v42
	v_cvt_pk_bf16_f32 v35, v47, v43
	v_cvt_pk_bf16_f32 v36, v46, v44
	s_waitcnt lgkmcnt(0)
	v_cvt_pk_bf16_f32 v37, v45, v49
	ds_read_b32 v42, v112 offset:1124
	ds_read_b32 v43, v112 offset:3180
	ds_read_b32 v44, v112 offset:5236
	ds_read_b32 v45, v112 offset:6264
	ds_read_b32 v46, v112 offset:4208
	ds_read_b32 v47, v112 offset:2152
	ds_read_b32 v48, v112 offset:96
	ds_read_b32 v49, v112 offset:7292
	v_mov_b32_e32 v109, v101
	global_store_dwordx4 v[40:41], v[34:37], off nt
	v_lshl_add_u64 v[38:39], v[38:39], 0, v[108:109]
	v_mov_b64_e32 v[56:57], v[32:33]
	s_waitcnt lgkmcnt(1)
	v_cvt_pk_bf16_f32 v34, v48, v42
	v_cvt_pk_bf16_f32 v35, v47, v43
	v_cvt_pk_bf16_f32 v36, v46, v44
	s_waitcnt lgkmcnt(0)
	v_cvt_pk_bf16_f32 v37, v45, v49
	global_store_dwordx4 v[38:39], v[34:37], off nt
	v_mov_b64_e32 v[60:61], v[28:29]
	v_mov_b64_e32 v[52:53], v[20:21]
	v_mov_b64_e32 v[40:41], v[12:13]
	v_mov_b64_e32 v[48:49], v[16:17]
	v_mov_b64_e32 v[36:37], v[4:5]
	v_mov_b64_e32 v[44:45], v[8:9]
	v_mov_b64_e32 v[64:65], v[24:25]
	v_mov_b64_e32 v[54:55], v[30:31]
	v_mov_b64_e32 v[58:59], v[26:27]
	v_mov_b64_e32 v[50:51], v[18:19]
	v_mov_b64_e32 v[38:39], v[10:11]
	v_mov_b64_e32 v[46:47], v[14:15]
	v_mov_b64_e32 v[34:35], v[2:3]
	v_mov_b64_e32 v[42:43], v[6:7]
	v_mov_b64_e32 v[62:63], v[22:23]
	v_mov_b64_e32 v[30:31], v[94:95]
	v_mov_b64_e32 v[26:27], v[90:91]
	v_mov_b64_e32 v[18:19], v[86:87]
	v_mov_b64_e32 v[10:11], v[82:83]
	v_mov_b64_e32 v[14:15], v[74:75]
	v_mov_b64_e32 v[2:3], v[66:67]
	v_mov_b64_e32 v[6:7], v[70:71]
	v_mov_b64_e32 v[22:23], v[78:79]
	s_cmpk_lt_i32 s7, 0xaf6
	v_mov_b64_e32 v[32:33], v[96:97]
	v_mov_b64_e32 v[28:29], v[92:93]
	v_mov_b64_e32 v[20:21], v[88:89]
	v_mov_b64_e32 v[12:13], v[84:85]
	v_mov_b64_e32 v[16:17], v[76:77]
	v_mov_b64_e32 v[4:5], v[68:69]
	v_mov_b64_e32 v[8:9], v[72:73]
	v_mov_b64_e32 v[24:25], v[80:81]
	s_mov_b32 s3, s7
	s_cbranch_scc0 .LBB0_78
.LBB0_76:
	s_add_i32 s7, s6, s3
	s_cmpk_gt_i32 s7, 0xaf5
	s_cbranch_scc1 .LBB0_75
	s_ashr_i32 s8, s7, 31
	s_lshr_b32 s8, s8, 26
	s_add_i32 s9, s7, s8
	s_ashr_i32 s8, s9, 6
	s_and_b32 s9, s9, 0xffc0
	s_sub_i32 s7, s7, s9
	s_bfe_i32 s9, s7, 0x80000
	s_bfe_u32 s9, s9, 0x2000d
	s_add_i32 s9, s7, s9
	s_bfe_i32 s10, s9, 0x80000
	s_and_b32 s9, s9, 0xfc
	s_sub_i32 s7, s7, s9
	s_ashr_i32 s9, s8, 31
	s_lshl_b64 s[8:9], s[8:9], 22
	s_sext_i32_i16 s10, s10
	s_sext_i32_i8 s7, s7
	s_add_u32 s8, s72, s8
	v_lshl_or_b32 v66, s7, 8, v99
	s_addc_u32 s9, s73, s9
	s_lshl_b32 s7, s10, 4
	s_andn2_b32 s7, s7, 63
	v_or_b32_e32 v68, s7, v110
	v_ashrrev_i32_e32 v69, 31, v68
	v_lshlrev_b64 v[68:69], 12, v[68:69]
	v_lshl_add_u64 v[68:69], s[8:9], 0, v[68:69]
	v_ashrrev_i32_e32 v67, 31, v66
	v_lshl_add_u64 v[90:91], v[66:67], 2, v[68:69]
	v_add_co_u32_e32 v66, vcc, s0, v90
	s_nop 1
	v_addc_co_u32_e32 v67, vcc, 0, v91, vcc
	v_add_co_u32_e32 v74, vcc, s1, v90
	global_load_dwordx4 v[70:73], v[66:67], off offset:-4096 nt
	s_nop 0
	global_load_dwordx4 v[66:69], v[66:67], off nt
	v_addc_co_u32_e32 v75, vcc, 0, v91, vcc
	v_add_co_u32_e32 v82, vcc, 0x4000, v90
	global_load_dwordx4 v[78:81], v[90:91], off nt
	s_nop 0
	global_load_dwordx4 v[74:77], v[74:75], off nt
	v_addc_co_u32_e32 v83, vcc, 0, v91, vcc
	v_add_co_u32_e32 v86, vcc, 0x5000, v90
	s_nop 1
	v_addc_co_u32_e32 v87, vcc, 0, v91, vcc
	v_add_co_u32_e32 v92, vcc, 0x6000, v90
	global_load_dwordx4 v[82:85], v[82:83], off nt
	s_nop 0
	global_load_dwordx4 v[86:89], v[86:87], off nt
	v_addc_co_u32_e32 v93, vcc, 0, v91, vcc
	v_add_co_u32_e32 v94, vcc, 0x7000, v90
	s_nop 1
	v_addc_co_u32_e32 v95, vcc, 0, v91, vcc
	global_load_dwordx4 v[90:93], v[92:93], off nt
	s_nop 0
	global_load_dwordx4 v[94:97], v[94:95], off nt
	s_branch .LBB0_75

; #define SEAM(k) do { if (IN(k) && IN((k) + 1)) xcd_barrier(bar); \
;         if (PROBE_MASK) { const unsigned long long t_ = __builtin_amdgcn_s_memrealtime(); if ((PROBE_MASK >> (k)) & 1u) pr_acc += t_ - pr_t0; pr_t0 = t_; } } while (0)
; __device__ __forceinline__ void convert_deferred(const Ptrs& P, unsigned char* lds, int quota) {
;     const int tid = threadIdx.x, wid = tid >> 6, lane = tid & 63;
;     float* tile = (float*)lds;
;     volatile __attribute__((address_space(3))) int* slot = (volatile __attribute__((address_space(3))) int*)((__attribute__((address_space(3))) unsigned char*)lds + 131072 + 320 + 11000);
;     unsigned* q = (unsigned*)(P.ws + WS_CTL) + CW_DEFQ;
;     for (int n = 0; n < quota; ++n) {
;         __syncthreads();
;         if (tid == 0) *slot = (int)atomicAdd(q, 1u);
;         __syncthreads();
;         const int t = *slot;
;         if (t >= DEF_GU + DEF_DN) break;
;         const bool gu = t < DEF_GU;
;         const float* src = gu ? P.in[34] : P.in[36]; bf16* dst = (bf16*)(P.ws + (gu ? WS_WGU : WS_WDN));
;         const int N = gu ? 2048 : 1024, ntn = N / 256, it = gu ? 2 * NE * 16 * 8 - DEF_GU + t : 2 * NE * 16 * 4 - DEF_DN + (t - DEF_GU);
; __global__ void __launch_bounds__(NT, 2) mega(Args args) {
;     ...
;     if (IN(2)) { g8::DenseOrder S; S.init(H, D, (const bf16*)(ws + WS_WEVIN), D, R, EVEN_IN_P, G, (int)blockIdx.x, 0); g8::EpiStoreBf16 E{Z, EVEN_IN_P};
;         g8::gemm_phase<g8::EpiStoreBf16, g8::DenseOrder, false, true>(LDSP, D, D, S, E);
;         if (IDLE_LAST(68 * 7)) convert_deferred(P, lds, 4); } SEAM(2);
.LBB0_779:
	s_abs_i32 s3, s62
	v_cvt_f32_u32_e32 v2, s3
	s_sub_i32 s4, 0, s3
	s_mov_b32 s5, 0
	v_rcp_iflag_f32_e32 v2, v2
	s_nop 0
	v_mul_f32_e32 v2, 0x4f7ffffe, v2
	v_cvt_u32_f32_e32 v2, v2
	s_nop 0
	v_readfirstlane_b32 s6, v2
	s_mul_i32 s4, s4, s6
	s_mul_hi_u32 s4, s6, s4
	s_add_i32 s6, s6, s4
	s_mul_hi_u32 s4, s6, 0x1dc
	s_mul_i32 s4, s4, s3
	s_sub_i32 s4, 0x1dc, s4
	s_sub_i32 s6, s4, s3
	s_cmp_ge_u32 s4, s3
	s_cselect_b32 s4, s6, s4
	s_sub_i32 s6, s4, s3
	s_cmp_ge_u32 s4, s3
	s_cselect_b32 s3, s6, s4
	s_cmp_eq_u32 s3, 0
	s_cselect_b64 s[6:7], -1, 0
	s_cmp_lt_i32 s2, s3
	s_cselect_b64 s[8:9], -1, 0
	s_or_b64 s[6:7], s[6:7], s[8:9]
	s_and_b64 vcc, exec, s[6:7]
	s_cbranch_vccnz .LBB0_789
	v_and_b32_e32 v2, 0x7c, v155
	v_lshlrev_b32_e32 v3, 5, v0
	s_movk_i32 s3, 0x400
	v_lshrrev_b32_e32 v4, 6, v0
	v_and_or_b32 v12, v3, s3, v2
	v_bfe_u32 v2, v0, 3, 3
	v_lshl_or_b32 v5, v4, 5, v2
	v_lshlrev_b32_e32 v2, 3, v0
	v_lshl_add_u32 v11, v182, 4, 0
	v_and_b32_e32 v2, 56, v2
	v_mul_u32_u24_e32 v16, 0x2020, v4
	v_mov_b32_e32 v3, 0
	v_lshl_add_u32 v27, v5, 2, 0
	v_mul_u32_u24_e32 v28, 0x404, v2
	v_lshlrev_b32_e32 v10, 6, v5
	s_add_i32 s12, 0, 0x22c38
	v_add_u32_e32 v16, v11, v16
	v_and_b32_e32 v13, 0xfc, v155
	v_and_b32_e32 v14, 56, v154
	s_mov_b32 s3, 8
	v_or_b32_e32 v4, 0x200, v10
	v_mov_b32_e32 v5, v3
	v_or_b32_e32 v6, 0x400, v10
	v_mov_b32_e32 v7, v3
	v_or_b32_e32 v8, 0x600, v10
	v_mov_b32_e32 v9, v3
	v_mov_b32_e32 v15, s12
	s_movk_i32 s13, 0xff9
	s_movk_i32 s14, 0x800
	s_mov_b32 s15, 0x1104e000
	s_movk_i32 s16, 0x6
	v_add_u32_e32 v17, 0x404, v16
	v_add_u32_e32 v18, 0x40c, v16
	v_add_u32_e32 v19, 0x808, v16
	v_add_u32_e32 v20, 0xc0c, v16
	v_add_u32_e32 v21, 0xc14, v16
	v_add_u32_e32 v22, 0x1414, v16
	v_add_u32_e32 v23, 0x141c, v16
	v_add_u32_e32 v24, 0x1818, v16
	v_add_u32_e32 v25, 0x1c1c, v16
	v_add_u32_e32 v26, 0x1c24, v16
	v_lshlrev_b32_e32 v2, 1, v2
	v_add_u32_e32 v27, v27, v28
	v_lshlrev_b32_e32 v10, 1, v10
	s_branch .LBB0_782

; __device__ __forceinline__ unsigned g8_cvt_pk(float lo, float hi) { unsigned r; asm volatile("v_cvt_pk_bf16_f32 %0, %1, %2" : "=v"(r) : "v"(lo), "v"(hi)); return r; }
; __device__ __forceinline__ void convert_deferred(const Ptrs& P, unsigned char* lds, int quota) {
;     ...
;         __syncthreads();
;         if (tid == 0) *slot = (int)atomicAdd(q, 1u);
;         __syncthreads();
;         const int t = *slot;
;         if (t >= DEF_GU + DEF_DN) break;
;         const bool gu = t < DEF_GU;
;         const float* src = gu ? P.in[34] : P.in[36]; bf16* dst = (bf16*)(P.ws + (gu ? WS_WGU : WS_WDN));
;         const int N = gu ? 2048 : 1024, ntn = N / 256, it = gu ? 2 * NE * 16 * 8 - DEF_GU + t : 2 * NE * 16 * 4 - DEF_DN + (t - DEF_GU);
;         f32x4 cur[8];
;         bt_load(src, N, gu ? 1 : 0, it, ntn, cur);
; #pragma unroll
;         for (int i = 0; i < 8; ++i) { float* tp = tile + (wid * 8 + i) * 257 + lane * 4; tp[0] = cur[i][0]; tp[1] = cur[i][1]; tp[2] = cur[i][2]; tp[3] = cur[i][3]; }
;         __syncthreads();
;         const int per = 16 * ntn, z = it / per, r = it % per, kt = r / ntn, nt = r % ntn;
;         bf16* d = dst + (size_t)z * N * 1024 + (((size_t)nt * 16 + kt) << 14);
;         const int kc = lane & 7;
; #pragma unroll
;         for (int pss = 0; pss < 4; ++pss) {
;             const int nn = wid * 32 + pss * 8 + (lane >> 3); float f[8];
; #pragma unroll
;             for (int j = 0; j < 8; ++j) f[j] = tile[(kc * 8 + j) * 257 + nn];
;             u32x4 w; w.x = g8_cvt_pk(f[0], f[1]); w.y = g8_cvt_pk(f[2], f[3]); w.z = g8_cvt_pk(f[4], f[5]); w.w = g8_cvt_pk(f[6], f[7]);
;             *(u32x4*)(d + nn * 64 + kc * 8) = w;
;         }
.LBB0_786:
	s_or_b64 exec, exec, s[6:7]
	s_waitcnt lgkmcnt(0)
	s_barrier
	ds_read_b32 v11, v15
	s_mov_b64 s[6:7], -1
	s_waitcnt lgkmcnt(0)
	v_cmp_lt_i32_e32 vcc, s13, v11
	v_readfirstlane_b32 s4, v11
	s_cbranch_vccnz .LBB0_781
	s_cmpk_gt_i32 s4, 0xaef
	s_cselect_b64 vcc, -1, 0
	s_and_b64 s[6:7], vcc, exec
	s_cselect_b32 s6, s15, 0x104e000
	s_cselect_b32 s11, 0x400, s14
	s_cselect_b32 s17, s73, s69
	s_cselect_b32 s20, s72, s68
	s_cselect_b32 s7, s16, 0x1510
	s_cselect_b32 s18, 20, 21
	s_cselect_b32 s21, 10, 11
	s_add_u32 s26, s78, s6
	s_addc_u32 s27, s79, 0
	s_lshr_b32 s8, s11, 4
	s_abs_i32 s6, s8
	v_cvt_f32_u32_e32 v11, s6
	s_sub_i32 s19, 0, s6
	s_add_i32 s7, s7, s4
	s_abs_i32 s9, s7
	v_rcp_iflag_f32_e32 v11, v11
	s_xor_b32 s4, s7, s8
	s_lshr_b32 s10, s11, 8
	s_ashr_i32 s4, s4, 31
	v_mul_f32_e32 v11, 0x4f7ffffe, v11
	v_cvt_u32_f32_e32 v11, v11
	s_nop 0
	v_readfirstlane_b32 s28, v11
	s_mul_i32 s19, s19, s28
	s_mul_hi_u32 s19, s28, s19
	s_add_i32 s28, s28, s19
	s_mul_hi_u32 s19, s9, s28
	s_mul_i32 s28, s19, s6
	s_sub_i32 s9, s9, s28
	s_add_i32 s28, s19, 1
	s_sub_i32 s29, s9, s6
	s_cmp_ge_u32 s9, s6
	s_cselect_b32 s19, s28, s19
	s_cselect_b32 s9, s29, s9
	s_add_i32 s28, s19, 1
	s_cmp_ge_u32 s9, s6
	s_cselect_b32 s6, s28, s19
	s_xor_b32 s6, s6, s4
	s_sub_i32 s6, s6, s4
	s_sext_i32_i8 s4, s10
	v_cvt_f32_i32_e32 v11, s4
	s_mul_i32 s8, s6, s8
	s_sub_i32 s7, s7, s8
	v_cvt_f32_i32_e32 v28, s7
	v_rcp_iflag_f32_e32 v29, v11
	s_xor_b32 s4, s7, s4
	s_ashr_i32 s4, s4, 30
	s_or_b32 s4, s4, 1
	v_mul_f32_e32 v29, v28, v29
	v_trunc_f32_e32 v29, v29
	v_fma_f32 v28, -v29, v11, v28
	v_cvt_i32_f32_e32 v29, v29
	v_cmp_ge_f32_e64 s[8:9], |v28|, |v11|
	s_and_b64 s[8:9], s[8:9], exec
	s_cselect_b32 s4, s4, 0
	v_readfirstlane_b32 s8, v29
	s_add_i32 s8, s8, s4
	s_mul_i32 s9, s8, s10
	s_sub_i32 s10, s7, s9
	s_sext_i32_i8 s7, s10
	v_lshl_add_u32 v11, s7, 7, v12
	v_lshl_or_b32 v28, s7, 8, v13
	s_ashr_i32 s7, s6, 31
	s_sext_i32_i8 s4, s8
	s_lshl_b64 s[18:19], s[6:7], s18
	v_lshl_or_b32 v30, s4, 6, v14
	s_lshl_b64 s[18:19], s[18:19], 2
	v_ashrrev_i32_e32 v31, 31, v30
	s_add_u32 s18, s20, s18
	v_cndmask_b32_e32 v28, v11, v28, vcc
	s_addc_u32 s19, s17, s19
	v_lshlrev_b64 v[30:31], s21, v[30:31]
	v_lshl_add_u64 v[30:31], v[30:31], 2, s[18:19]
	v_ashrrev_i32_e32 v29, 31, v28
	v_lshl_add_u64 v[52:53], v[28:29], 2, v[30:31]
	s_lshl_b64 s[18:19], 12, s21
	s_lshl_b32 s4, s11, 2
	v_lshl_add_u64 v[40:41], v[52:53], 0, s[18:19]
	s_lshl_b64 s[18:19], 24, s21
	v_lshl_add_u64 v[36:37], v[52:53], 0, s[4:5]
	v_lshl_add_u64 v[44:45], v[52:53], 0, s[18:19]
	s_lshl_b64 s[18:19], 28, s21
	v_lshl_add_u64 v[54:55], v[36:37], 0, s[4:5]
	v_lshl_add_u64 v[48:49], v[52:53], 0, s[18:19]
	s_lshl_b32 s4, s11, 3
	s_lshl_b64 s[18:19], 20, s21
	global_load_dwordx4 v[28:31], v[52:53], off nt
	global_load_dwordx4 v[32:35], v[36:37], off nt
	s_nop 0
	global_load_dwordx4 v[36:39], v[54:55], off nt
	s_nop 0
	global_load_dwordx4 v[40:43], v[40:41], off nt
	v_lshl_add_u64 v[54:55], v[54:55], 0, s[4:5]
	v_lshl_add_u64 v[56:57], v[52:53], 0, s[18:19]
	global_load_dwordx4 v[44:47], v[44:45], off nt
	s_nop 0
	global_load_dwordx4 v[48:51], v[48:49], off nt
	s_nop 0
	global_load_dwordx4 v[52:55], v[54:55], off nt
	s_nop 0
	global_load_dwordx4 v[56:59], v[56:57], off nt
	s_lshl_b64 s[6:7], s[6:7], s21
	s_lshl_b64 s[6:7], s[6:7], 11
	s_add_u32 s4, s26, s6
	s_addc_u32 s11, s27, s7
	s_bfe_i64 s[6:7], s[10:11], 0x80000
	s_bfe_i64 s[8:9], s[8:9], 0x80000
	s_lshl_b64 s[6:7], s[6:7], 19
	s_add_u32 s4, s4, s6
	s_addc_u32 s10, s11, s7
	s_lshl_b64 s[6:7], s[8:9], 15
	s_add_u32 s6, s4, s6
	s_addc_u32 s7, s10, s7
	v_mov_b32_e32 v11, v3
	s_add_i32 s3, s3, -1
	s_cmp_eq_u32 s3, 0
	s_waitcnt vmcnt(7)
	ds_write_b128 v16, v[28:31]
	s_waitcnt vmcnt(6)
	ds_write2_b32 v17, v32, v33 offset1:1
	ds_write2_b32 v18, v34, v35 offset1:1
	s_waitcnt vmcnt(3)
	ds_write2_b64 v24, v[44:45], v[46:47] offset1:1
	s_waitcnt vmcnt(2)
	ds_write2_b32 v25, v48, v49 offset1:1
	ds_write2_b32 v26, v50, v51 offset1:1
	ds_write2_b64 v19, v[36:37], v[38:39] offset1:1
	ds_write2_b32 v20, v40, v41 offset1:1
	ds_write2_b32 v21, v42, v43 offset1:1
	s_waitcnt vmcnt(1)
	ds_write_b128 v16, v[52:55] offset:4112
	s_waitcnt vmcnt(0)
	ds_write2_b32 v22, v56, v57 offset1:1
	ds_write2_b32 v23, v58, v59 offset1:1
	s_waitcnt lgkmcnt(0)
	s_barrier
	ds_read_b32 v28, v27 offset:1028
	ds_read_b32 v29, v27 offset:3084
	ds_read_b32 v30, v27 offset:5140
	ds_read_b32 v31, v27 offset:7196
	ds_read_b32 v32, v27 offset:6168
	ds_read_b32 v33, v27 offset:4112
	ds_read_b32 v34, v27 offset:2056
	ds_read_b32 v35, v27
	s_waitcnt lgkmcnt(0)
	v_cvt_pk_bf16_f32 v28, v35, v28
	v_cvt_pk_bf16_f32 v29, v34, v29
	v_cvt_pk_bf16_f32 v30, v33, v30
	v_cvt_pk_bf16_f32 v31, v32, v31
	ds_read_b32 v36, v27 offset:1060
	ds_read_b32 v37, v27 offset:3116
	ds_read_b32 v38, v27 offset:5172
	ds_read_b32 v39, v27 offset:7228
	ds_read_b32 v40, v27 offset:6200
	ds_read_b32 v41, v27 offset:4144
	ds_read_b32 v42, v27 offset:2088
	ds_read_b32 v43, v27 offset:32
	v_lshl_add_u64 v[32:33], s[6:7], 0, v[2:3]
	v_lshl_add_u64 v[34:35], v[32:33], 0, v[10:11]
	global_store_dwordx4 v[34:35], v[28:31], off
	v_lshl_add_u64 v[34:35], v[4:5], 1, v[32:33]
	s_cselect_b64 s[6:7], -1, 0
	s_waitcnt lgkmcnt(0)
	v_cvt_pk_bf16_f32 v28, v43, v36
	v_cvt_pk_bf16_f32 v29, v42, v37
	v_cvt_pk_bf16_f32 v30, v41, v38
	v_cvt_pk_bf16_f32 v31, v40, v39
	ds_read_b32 v11, v27 offset:1092
	ds_read_b32 v36, v27 offset:3148
	ds_read_b32 v37, v27 offset:6232
	ds_read_b32 v38, v27 offset:4176
	ds_read_b32 v39, v27 offset:2120
	ds_read_b32 v40, v27 offset:64
	ds_read_b32 v41, v27 offset:5204
	ds_read_b32 v42, v27 offset:7260
	global_store_dwordx4 v[34:35], v[28:31], off
	v_lshl_add_u64 v[34:35], v[6:7], 1, v[32:33]
	v_lshl_add_u64 v[32:33], v[8:9], 1, v[32:33]
	s_waitcnt lgkmcnt(2)
	v_cvt_pk_bf16_f32 v28, v40, v11
	v_cvt_pk_bf16_f32 v29, v39, v36
	s_waitcnt lgkmcnt(1)
	v_cvt_pk_bf16_f32 v30, v38, v41
	s_waitcnt lgkmcnt(0)
	v_cvt_pk_bf16_f32 v31, v37, v42
	ds_read_b32 v11, v27 offset:1124
	ds_read_b32 v36, v27 offset:3180
	ds_read_b32 v37, v27 offset:6264
	ds_read_b32 v38, v27 offset:4208
	ds_read_b32 v39, v27 offset:2152
	ds_read_b32 v40, v27 offset:96
	ds_read_b32 v41, v27 offset:5236
	ds_read_b32 v42, v27 offset:7292
	global_store_dwordx4 v[34:35], v[28:31], off
	s_waitcnt lgkmcnt(2)
	s_nop 0
	v_cvt_pk_bf16_f32 v28, v40, v11
	v_cvt_pk_bf16_f32 v29, v39, v36
	s_waitcnt lgkmcnt(1)
	v_cvt_pk_bf16_f32 v30, v38, v41
	s_waitcnt lgkmcnt(0)
	v_cvt_pk_bf16_f32 v31, v37, v42
	global_store_dwordx4 v[32:33], v[28:31], off
	s_branch .LBB0_781

; #define SEAM(k) do { if (IN(k) && IN((k) + 1)) xcd_barrier(bar); \
;         if (PROBE_MASK) { const unsigned long long t_ = __builtin_amdgcn_s_memrealtime(); if ((PROBE_MASK >> (k)) & 1u) pr_acc += t_ - pr_t0; pr_t0 = t_; } } while (0)
; __device__ __forceinline__ void convert_deferred(const Ptrs& P, unsigned char* lds, int quota) {
;     const int tid = threadIdx.x, wid = tid >> 6, lane = tid & 63;
;     float* tile = (float*)lds;
;     volatile __attribute__((address_space(3))) int* slot = (volatile __attribute__((address_space(3))) int*)((__attribute__((address_space(3))) unsigned char*)lds + 131072 + 320 + 11000);
;     unsigned* q = (unsigned*)(P.ws + WS_CTL) + CW_DEFQ;
;     for (int n = 0; n < quota; ++n) {
;         __syncthreads();
;         if (tid == 0) *slot = (int)atomicAdd(q, 1u);
;         __syncthreads();
;         const int t = *slot;
;         if (t >= DEF_GU + DEF_DN) break;
;         const bool gu = t < DEF_GU;
;         const float* src = gu ? P.in[34] : P.in[36]; bf16* dst = (bf16*)(P.ws + (gu ? WS_WGU : WS_WDN));
;         const int N = gu ? 2048 : 1024, ntn = N / 256, it = gu ? 2 * NE * 16 * 8 - DEF_GU + t : 2 * NE * 16 * 4 - DEF_DN + (t - DEF_GU);
; __global__ void __launch_bounds__(NT, 2) mega(Args args) {
;     ...
;     if (IN(6)) { g8::DenseOrder S; S.init(MIX, D, (const bf16*)(ws + WS_WEVOUT), D, R, D, G, (int)blockIdx.x, 0); g8::EpiOut E{P, 0};
;         g8::gemm_phase<g8::EpiOut, g8::DenseOrder, false, true>(LDSP, D, D, S, E);
;         if (IDLE_LAST(68 * 4)) convert_deferred(P, lds, 4); } SEAM(6);
.LBB0_1286:
	s_abs_i32 s3, s62
	v_cvt_f32_u32_e32 v2, s3
	s_sub_i32 s4, 0, s3
	s_mov_b32 s5, 0
	v_rcp_iflag_f32_e32 v2, v2
	s_nop 0
	v_mul_f32_e32 v2, 0x4f7ffffe, v2
	v_cvt_u32_f32_e32 v2, v2
	s_nop 0
	v_readfirstlane_b32 s6, v2
	s_mul_i32 s4, s4, s6
	s_mul_hi_u32 s4, s6, s4
	s_add_i32 s6, s6, s4
	s_mul_hi_u32 s4, s6, 0x110
	s_mul_i32 s4, s4, s3
	s_sub_i32 s4, 0x110, s4
	s_sub_i32 s6, s4, s3
	s_cmp_ge_u32 s4, s3
	s_cselect_b32 s4, s6, s4
	s_sub_i32 s6, s4, s3
	s_cmp_ge_u32 s4, s3
	s_cselect_b32 s3, s6, s4
	s_cmp_eq_u32 s3, 0
	s_cselect_b64 s[6:7], -1, 0
	s_cmp_lt_i32 s2, s3
	s_cselect_b64 s[8:9], -1, 0
	s_or_b64 s[6:7], s[6:7], s[8:9]
	s_and_b64 vcc, exec, s[6:7]
	s_cbranch_vccnz .LBB0_1296
	v_and_b32_e32 v2, 0x7c, v188
	v_lshlrev_b32_e32 v3, 5, v0
	s_movk_i32 s3, 0x400
	v_and_or_b32 v12, v3, s3, v2
	v_bfe_u32 v2, v0, 3, 3
	v_lshl_or_b32 v4, v1, 5, v2
	v_lshlrev_b32_e32 v2, 3, v0
	v_lshl_add_u32 v11, v182, 4, 0
	v_and_b32_e32 v2, 56, v2
	v_mul_u32_u24_e32 v16, 0x2020, v1
	v_mov_b32_e32 v3, 0
	v_lshl_add_u32 v27, v4, 2, 0
	v_mul_u32_u24_e32 v28, 0x404, v2
	v_lshlrev_b32_e32 v10, 6, v4
	s_add_i32 s12, 0, 0x22c38
	v_add_u32_e32 v16, v11, v16
	v_and_b32_e32 v13, 0xfc, v188
	v_and_b32_e32 v14, 56, v185
	s_mov_b32 s3, 10
	v_or_b32_e32 v4, 0x200, v10
	v_mov_b32_e32 v5, v3
	v_or_b32_e32 v6, 0x400, v10
	v_mov_b32_e32 v7, v3
	v_or_b32_e32 v8, 0x600, v10
	v_mov_b32_e32 v9, v3
	v_mov_b32_e32 v15, s12
	s_movk_i32 s13, 0xff9
	s_movk_i32 s14, 0x800
	s_mov_b32 s15, 0x1104e000
	s_movk_i32 s16, 0x6
	v_add_u32_e32 v17, 0x404, v16
	v_add_u32_e32 v18, 0x40c, v16
	v_add_u32_e32 v19, 0x808, v16
	v_add_u32_e32 v20, 0xc0c, v16
	v_add_u32_e32 v21, 0xc14, v16
	v_add_u32_e32 v22, 0x1414, v16
	v_add_u32_e32 v23, 0x141c, v16
	v_add_u32_e32 v24, 0x1818, v16
	v_add_u32_e32 v25, 0x1c1c, v16
	v_add_u32_e32 v26, 0x1c24, v16
	v_lshlrev_b32_e32 v2, 1, v2
	v_add_u32_e32 v27, v27, v28
	v_lshlrev_b32_e32 v10, 1, v10
	s_branch .LBB0_1289

; __device__ __forceinline__ unsigned g8_cvt_pk(float lo, float hi) { unsigned r; asm volatile("v_cvt_pk_bf16_f32 %0, %1, %2" : "=v"(r) : "v"(lo), "v"(hi)); return r; }
; __device__ __forceinline__ void convert_deferred(const Ptrs& P, unsigned char* lds, int quota) {
;     ...
;         __syncthreads();
;         if (tid == 0) *slot = (int)atomicAdd(q, 1u);
;         __syncthreads();
;         const int t = *slot;
;         if (t >= DEF_GU + DEF_DN) break;
;         const bool gu = t < DEF_GU;
;         const float* src = gu ? P.in[34] : P.in[36]; bf16* dst = (bf16*)(P.ws + (gu ? WS_WGU : WS_WDN));
;         const int N = gu ? 2048 : 1024, ntn = N / 256, it = gu ? 2 * NE * 16 * 8 - DEF_GU + t : 2 * NE * 16 * 4 - DEF_DN + (t - DEF_GU);
;         f32x4 cur[8];
;         bt_load(src, N, gu ? 1 : 0, it, ntn, cur);
; #pragma unroll
;         for (int i = 0; i < 8; ++i) { float* tp = tile + (wid * 8 + i) * 257 + lane * 4; tp[0] = cur[i][0]; tp[1] = cur[i][1]; tp[2] = cur[i][2]; tp[3] = cur[i][3]; }
;         __syncthreads();
;         const int per = 16 * ntn, z = it / per, r = it % per, kt = r / ntn, nt = r % ntn;
;         bf16* d = dst + (size_t)z * N * 1024 + (((size_t)nt * 16 + kt) << 14);
;         const int kc = lane & 7;
; #pragma unroll
;         for (int pss = 0; pss < 4; ++pss) {
;             const int nn = wid * 32 + pss * 8 + (lane >> 3); float f[8];
; #pragma unroll
;             for (int j = 0; j < 8; ++j) f[j] = tile[(kc * 8 + j) * 257 + nn];
;             u32x4 w; w.x = g8_cvt_pk(f[0], f[1]); w.y = g8_cvt_pk(f[2], f[3]); w.z = g8_cvt_pk(f[4], f[5]); w.w = g8_cvt_pk(f[6], f[7]);
;             *(u32x4*)(d + nn * 64 + kc * 8) = w;
;         }
.LBB0_1293:
	s_or_b64 exec, exec, s[6:7]
	s_waitcnt lgkmcnt(0)
	s_barrier
	ds_read_b32 v11, v15
	s_mov_b64 s[6:7], -1
	s_waitcnt lgkmcnt(0)
	v_cmp_lt_i32_e32 vcc, s13, v11
	v_readfirstlane_b32 s4, v11
	s_cbranch_vccnz .LBB0_1288
	s_cmpk_gt_i32 s4, 0xaef
	s_cselect_b64 vcc, -1, 0
	s_and_b64 s[6:7], vcc, exec
	s_cselect_b32 s6, s15, 0x104e000
	s_cselect_b32 s11, 0x400, s14
	s_cselect_b32 s17, s73, s69
	s_cselect_b32 s20, s72, s68
	s_cselect_b32 s7, s16, 0x1510
	s_cselect_b32 s18, 20, 21
	s_cselect_b32 s21, 10, 11
	s_add_u32 s22, s78, s6
	s_addc_u32 s23, s79, 0
	s_lshr_b32 s8, s11, 4
	s_abs_i32 s6, s8
	v_cvt_f32_u32_e32 v11, s6
	s_sub_i32 s19, 0, s6
	s_add_i32 s7, s7, s4
	s_abs_i32 s9, s7
	v_rcp_iflag_f32_e32 v11, v11
	s_xor_b32 s4, s7, s8
	s_lshr_b32 s10, s11, 8
	s_ashr_i32 s4, s4, 31
	v_mul_f32_e32 v11, 0x4f7ffffe, v11
	v_cvt_u32_f32_e32 v11, v11
	s_nop 0
	v_readfirstlane_b32 s24, v11
	s_mul_i32 s19, s19, s24
	s_mul_hi_u32 s19, s24, s19
	s_add_i32 s24, s24, s19
	s_mul_hi_u32 s19, s9, s24
	s_mul_i32 s24, s19, s6
	s_sub_i32 s9, s9, s24
	s_add_i32 s24, s19, 1
	s_sub_i32 s25, s9, s6
	s_cmp_ge_u32 s9, s6
	s_cselect_b32 s19, s24, s19
	s_cselect_b32 s9, s25, s9
	s_add_i32 s24, s19, 1
	s_cmp_ge_u32 s9, s6
	s_cselect_b32 s6, s24, s19
	s_xor_b32 s6, s6, s4
	s_sub_i32 s6, s6, s4
	s_sext_i32_i8 s4, s10
	v_cvt_f32_i32_e32 v11, s4
	s_mul_i32 s8, s6, s8
	s_sub_i32 s7, s7, s8
	v_cvt_f32_i32_e32 v28, s7
	v_rcp_iflag_f32_e32 v29, v11
	s_xor_b32 s4, s7, s4
	s_ashr_i32 s4, s4, 30
	s_or_b32 s4, s4, 1
	v_mul_f32_e32 v29, v28, v29
	v_trunc_f32_e32 v29, v29
	v_fma_f32 v28, -v29, v11, v28
	v_cvt_i32_f32_e32 v29, v29
	v_cmp_ge_f32_e64 s[8:9], |v28|, |v11|
	s_and_b64 s[8:9], s[8:9], exec
	s_cselect_b32 s4, s4, 0
	v_readfirstlane_b32 s8, v29
	s_add_i32 s8, s8, s4
	s_mul_i32 s9, s8, s10
	s_sub_i32 s10, s7, s9
	s_sext_i32_i8 s7, s10
	v_lshl_add_u32 v11, s7, 7, v12
	v_lshl_or_b32 v28, s7, 8, v13
	s_ashr_i32 s7, s6, 31
	s_sext_i32_i8 s4, s8
	s_lshl_b64 s[18:19], s[6:7], s18
	v_lshl_or_b32 v30, s4, 6, v14
	s_lshl_b64 s[18:19], s[18:19], 2
	v_ashrrev_i32_e32 v31, 31, v30
	s_add_u32 s18, s20, s18
	v_cndmask_b32_e32 v28, v11, v28, vcc
	s_addc_u32 s19, s17, s19
	v_lshlrev_b64 v[30:31], s21, v[30:31]
	v_lshl_add_u64 v[30:31], v[30:31], 2, s[18:19]
	v_ashrrev_i32_e32 v29, 31, v28
	v_lshl_add_u64 v[52:53], v[28:29], 2, v[30:31]
	s_lshl_b64 s[18:19], 12, s21
	s_lshl_b32 s4, s11, 2
	v_lshl_add_u64 v[40:41], v[52:53], 0, s[18:19]
	s_lshl_b64 s[18:19], 24, s21
	v_lshl_add_u64 v[36:37], v[52:53], 0, s[4:5]
	v_lshl_add_u64 v[44:45], v[52:53], 0, s[18:19]
	s_lshl_b64 s[18:19], 28, s21
	v_lshl_add_u64 v[54:55], v[36:37], 0, s[4:5]
	v_lshl_add_u64 v[48:49], v[52:53], 0, s[18:19]
	s_lshl_b32 s4, s11, 3
	s_lshl_b64 s[18:19], 20, s21
	global_load_dwordx4 v[28:31], v[52:53], off nt
	global_load_dwordx4 v[32:35], v[36:37], off nt
	s_nop 0
	global_load_dwordx4 v[36:39], v[54:55], off nt
	s_nop 0
	global_load_dwordx4 v[40:43], v[40:41], off nt
	v_lshl_add_u64 v[54:55], v[54:55], 0, s[4:5]
	v_lshl_add_u64 v[56:57], v[52:53], 0, s[18:19]
	global_load_dwordx4 v[44:47], v[44:45], off nt
	s_nop 0
	global_load_dwordx4 v[48:51], v[48:49], off nt
	s_nop 0
	global_load_dwordx4 v[52:55], v[54:55], off nt
	s_nop 0
	global_load_dwordx4 v[56:59], v[56:57], off nt
	s_lshl_b64 s[6:7], s[6:7], s21
	s_lshl_b64 s[6:7], s[6:7], 11
	s_add_u32 s4, s22, s6
	s_addc_u32 s11, s23, s7
	s_bfe_i64 s[6:7], s[10:11], 0x80000
	s_bfe_i64 s[8:9], s[8:9], 0x80000
	s_lshl_b64 s[6:7], s[6:7], 19
	s_add_u32 s4, s4, s6
	s_addc_u32 s10, s11, s7
	s_lshl_b64 s[6:7], s[8:9], 15
	s_add_u32 s6, s4, s6
	s_addc_u32 s7, s10, s7
	v_mov_b32_e32 v11, v3
	s_add_i32 s3, s3, -1
	s_cmp_eq_u32 s3, 0
	s_waitcnt vmcnt(7)
	ds_write_b128 v16, v[28:31]
	s_waitcnt vmcnt(6)
	ds_write2_b32 v17, v32, v33 offset1:1
	ds_write2_b32 v18, v34, v35 offset1:1
	s_waitcnt vmcnt(3)
	ds_write2_b64 v24, v[44:45], v[46:47] offset1:1
	s_waitcnt vmcnt(2)
	ds_write2_b32 v25, v48, v49 offset1:1
	ds_write2_b32 v26, v50, v51 offset1:1
	ds_write2_b64 v19, v[36:37], v[38:39] offset1:1
	ds_write2_b32 v20, v40, v41 offset1:1
	ds_write2_b32 v21, v42, v43 offset1:1
	s_waitcnt vmcnt(1)
	ds_write_b128 v16, v[52:55] offset:4112
	s_waitcnt vmcnt(0)
	ds_write2_b32 v22, v56, v57 offset1:1
	ds_write2_b32 v23, v58, v59 offset1:1
	s_waitcnt lgkmcnt(0)
	s_barrier
	ds_read_b32 v28, v27 offset:1028
	ds_read_b32 v29, v27 offset:3084
	ds_read_b32 v30, v27 offset:5140
	ds_read_b32 v31, v27 offset:7196
	ds_read_b32 v32, v27 offset:6168
	ds_read_b32 v33, v27 offset:4112
	ds_read_b32 v34, v27 offset:2056
	ds_read_b32 v35, v27
	s_waitcnt lgkmcnt(0)
	v_cvt_pk_bf16_f32 v28, v35, v28
	v_cvt_pk_bf16_f32 v29, v34, v29
	v_cvt_pk_bf16_f32 v30, v33, v30
	v_cvt_pk_bf16_f32 v31, v32, v31
	ds_read_b32 v36, v27 offset:1060
	ds_read_b32 v37, v27 offset:3116
	ds_read_b32 v38, v27 offset:5172
	ds_read_b32 v39, v27 offset:7228
	ds_read_b32 v40, v27 offset:6200
	ds_read_b32 v41, v27 offset:4144
	ds_read_b32 v42, v27 offset:2088
	ds_read_b32 v43, v27 offset:32
	v_lshl_add_u64 v[32:33], s[6:7], 0, v[2:3]
	v_lshl_add_u64 v[34:35], v[32:33], 0, v[10:11]
	global_store_dwordx4 v[34:35], v[28:31], off
	v_lshl_add_u64 v[34:35], v[4:5], 1, v[32:33]
	s_cselect_b64 s[6:7], -1, 0
	s_waitcnt lgkmcnt(0)
	v_cvt_pk_bf16_f32 v28, v43, v36
	v_cvt_pk_bf16_f32 v29, v42, v37
	v_cvt_pk_bf16_f32 v30, v41, v38
	v_cvt_pk_bf16_f32 v31, v40, v39
	ds_read_b32 v11, v27 offset:1092
	ds_read_b32 v36, v27 offset:3148
	ds_read_b32 v37, v27 offset:6232
	ds_read_b32 v38, v27 offset:4176
	ds_read_b32 v39, v27 offset:2120
	ds_read_b32 v40, v27 offset:64
	ds_read_b32 v41, v27 offset:5204
	ds_read_b32 v42, v27 offset:7260
	global_store_dwordx4 v[34:35], v[28:31], off
	v_lshl_add_u64 v[34:35], v[6:7], 1, v[32:33]
	v_lshl_add_u64 v[32:33], v[8:9], 1, v[32:33]
	s_waitcnt lgkmcnt(2)
	v_cvt_pk_bf16_f32 v28, v40, v11
	v_cvt_pk_bf16_f32 v29, v39, v36
	s_waitcnt lgkmcnt(1)
	v_cvt_pk_bf16_f32 v30, v38, v41
	s_waitcnt lgkmcnt(0)
	v_cvt_pk_bf16_f32 v31, v37, v42
	ds_read_b32 v11, v27 offset:1124
	ds_read_b32 v36, v27 offset:3180
	ds_read_b32 v37, v27 offset:6264
	ds_read_b32 v38, v27 offset:4208
	ds_read_b32 v39, v27 offset:2152
	ds_read_b32 v40, v27 offset:96
	ds_read_b32 v41, v27 offset:5236
	ds_read_b32 v42, v27 offset:7292
	global_store_dwordx4 v[34:35], v[28:31], off
	s_waitcnt lgkmcnt(2)
	s_nop 0
	v_cvt_pk_bf16_f32 v28, v40, v11
	v_cvt_pk_bf16_f32 v29, v39, v36
	s_waitcnt lgkmcnt(1)
	v_cvt_pk_bf16_f32 v30, v38, v41
	s_waitcnt lgkmcnt(0)
	v_cvt_pk_bf16_f32 v31, v37, v42
	global_store_dwordx4 v[32:33], v[28:31], off
	s_branch .LBB0_1288

; #define LAS __attribute__((address_space(3)))
; #define SEAM(k) do { if (IN(k) && IN((k) + 1)) xcd_barrier(bar); \
;         if (PROBE_MASK) { const unsigned long long t_ = __builtin_amdgcn_s_memrealtime(); if ((PROBE_MASK >> (k)) & 1u) pr_acc += t_ - pr_t0; pr_t0 = t_; } } while (0)
; __device__ __forceinline__ void convert_deferred(const Ptrs& P, unsigned char* lds, int quota) {
;     const int tid = threadIdx.x, wid = tid >> 6, lane = tid & 63;
;     float* tile = (float*)lds;
;     volatile __attribute__((address_space(3))) int* slot = (volatile __attribute__((address_space(3))) int*)((__attribute__((address_space(3))) unsigned char*)lds + 131072 + 320 + 11000);
;     unsigned* q = (unsigned*)(P.ws + WS_CTL) + CW_DEFQ;
;     for (int n = 0; n < quota; ++n) {
;         __syncthreads();
;         if (tid == 0) *slot = (int)atomicAdd(q, 1u);
;         __syncthreads();
;         const int t = *slot;
;         if (t >= DEF_GU + DEF_DN) break;
;         const bool gu = t < DEF_GU;
;         const float* src = gu ? P.in[34] : P.in[36]; bf16* dst = (bf16*)(P.ws + (gu ? WS_WGU : WS_WDN));
;         const int N = gu ? 2048 : 1024, ntn = N / 256, it = gu ? 2 * NE * 16 * 8 - DEF_GU + t : 2 * NE * 16 * 4 - DEF_DN + (t - DEF_GU);
; __global__ void __launch_bounds__(NT, 2) mega(Args args) {
;     ...
;     if (IN(9)) { g8::MoeOrder S{(const char*)(ws + WS_ACT), (const char*)(ws + WS_WDN) + (size_t)0 * NE * 1024 * 1024 * 2, nullptr, (size_t)1024 * 1024 * 2, 4, D, G, vcu, 0, nullptr};
;         S.init((const unsigned*)(ws + WS_CTL) + CW_CNT + 0 * 64, (LAS int*)(LDSP + MISC_OFF + 256)); g8::EpiMoe2 E{P, 0}; g8::gemm_phase<g8::EpiMoe2, g8::MoeOrder, false, true>(LDSP, D, D, S, E);
;         { const int rem_ = ((LAS int*)(LDSP + MISC_OFF + 256))[96] % G; if (rem_ != 0 && vcu >= rem_) convert_deferred(P, lds, 5); } } SEAM(9);
.LBB0_1609:
	s_abs_i32 s0, s62
	v_cvt_f32_u32_e32 v2, s0
	s_sub_i32 s5, 0, s0
	s_abs_i32 s4, s9
	s_ashr_i32 s3, s9, 31
	v_rcp_iflag_f32_e32 v2, v2
	s_mov_b32 s1, 0
	v_mul_f32_e32 v2, 0x4f7ffffe, v2
	v_cvt_u32_f32_e32 v2, v2
	s_nop 0
	v_readfirstlane_b32 s6, v2
	s_mul_i32 s5, s5, s6
	s_mul_hi_u32 s5, s6, s5
	s_add_i32 s6, s6, s5
	s_mul_hi_u32 s5, s4, s6
	s_mul_i32 s5, s5, s0
	s_sub_i32 s4, s4, s5
	s_sub_i32 s5, s4, s0
	s_cmp_ge_u32 s4, s0
	s_cselect_b32 s4, s5, s4
	s_sub_i32 s5, s4, s0
	s_cmp_ge_u32 s4, s0
	s_cselect_b32 s0, s5, s4
	s_xor_b32 s0, s0, s3
	s_sub_i32 s0, s0, s3
	s_cmp_eq_u32 s0, 0
	v_readlane_b32 s3, v254, 2
	s_cselect_b64 s[4:5], -1, 0
	s_cmp_lt_i32 s3, s0
	s_cselect_b64 s[6:7], -1, 0
	s_or_b64 s[4:5], s[4:5], s[6:7]
	s_and_b64 vcc, exec, s[4:5]
	s_cbranch_vccnz .LBB0_1619
	v_and_b32_e32 v2, 0x7c, v175
	v_lshlrev_b32_e32 v3, 5, v0
	s_movk_i32 s0, 0x400
	v_and_or_b32 v12, v3, s0, v2
	v_bfe_u32 v2, v0, 3, 3
	v_lshl_or_b32 v4, v1, 5, v2
	v_lshlrev_b32_e32 v2, 3, v0
	v_lshl_add_u32 v11, v182, 4, 0
	v_and_b32_e32 v2, 56, v2
	v_mul_u32_u24_e32 v16, 0x2020, v1
	v_mov_b32_e32 v3, 0
	v_lshl_add_u32 v27, v4, 2, 0
	v_mul_u32_u24_e32 v28, 0x404, v2
	v_lshlrev_b32_e32 v10, 6, v4
	s_add_i32 s10, 0, 0x22c38
	v_add_u32_e32 v16, v11, v16
	s_mov_b32 s3, 9
	v_and_b32_e32 v13, 0xfc, v175
	v_and_b32_e32 v14, 56, v173
	v_or_b32_e32 v4, 0x200, v10
	v_mov_b32_e32 v5, v3
	v_or_b32_e32 v6, 0x400, v10
	v_mov_b32_e32 v7, v3
	v_or_b32_e32 v8, 0x600, v10
	v_mov_b32_e32 v9, v3
	v_mov_b32_e32 v15, s10
	s_movk_i32 s11, 0xff9
	s_movk_i32 s12, 0x800
	s_mov_b32 s13, 0x1104e000
	s_movk_i32 s14, 0x6
	v_add_u32_e32 v17, 0x404, v16
	v_add_u32_e32 v18, 0x40c, v16
	v_add_u32_e32 v19, 0x808, v16
	v_add_u32_e32 v20, 0xc0c, v16
	v_add_u32_e32 v21, 0xc14, v16
	v_add_u32_e32 v22, 0x1414, v16
	v_add_u32_e32 v23, 0x141c, v16
	v_add_u32_e32 v24, 0x1818, v16
	v_add_u32_e32 v25, 0x1c1c, v16
	v_add_u32_e32 v26, 0x1c24, v16
	v_lshlrev_b32_e32 v2, 1, v2
	v_add_u32_e32 v27, v27, v28
	v_lshlrev_b32_e32 v10, 1, v10
	s_branch .LBB0_1612

; __device__ __forceinline__ unsigned g8_cvt_pk(float lo, float hi) { unsigned r; asm volatile("v_cvt_pk_bf16_f32 %0, %1, %2" : "=v"(r) : "v"(lo), "v"(hi)); return r; }
; __device__ __forceinline__ void convert_deferred(const Ptrs& P, unsigned char* lds, int quota) {
;     ...
;         __syncthreads();
;         if (tid == 0) *slot = (int)atomicAdd(q, 1u);
;         __syncthreads();
;         const int t = *slot;
;         if (t >= DEF_GU + DEF_DN) break;
;         const bool gu = t < DEF_GU;
;         const float* src = gu ? P.in[34] : P.in[36]; bf16* dst = (bf16*)(P.ws + (gu ? WS_WGU : WS_WDN));
;         const int N = gu ? 2048 : 1024, ntn = N / 256, it = gu ? 2 * NE * 16 * 8 - DEF_GU + t : 2 * NE * 16 * 4 - DEF_DN + (t - DEF_GU);
;         f32x4 cur[8];
;         bt_load(src, N, gu ? 1 : 0, it, ntn, cur);
; #pragma unroll
;         for (int i = 0; i < 8; ++i) { float* tp = tile + (wid * 8 + i) * 257 + lane * 4; tp[0] = cur[i][0]; tp[1] = cur[i][1]; tp[2] = cur[i][2]; tp[3] = cur[i][3]; }
;         __syncthreads();
;         const int per = 16 * ntn, z = it / per, r = it % per, kt = r / ntn, nt = r % ntn;
;         bf16* d = dst + (size_t)z * N * 1024 + (((size_t)nt * 16 + kt) << 14);
;         const int kc = lane & 7;
; #pragma unroll
;         for (int pss = 0; pss < 4; ++pss) {
;             const int nn = wid * 32 + pss * 8 + (lane >> 3); float f[8];
; #pragma unroll
;             for (int j = 0; j < 8; ++j) f[j] = tile[(kc * 8 + j) * 257 + nn];
;             u32x4 w; w.x = g8_cvt_pk(f[0], f[1]); w.y = g8_cvt_pk(f[2], f[3]); w.z = g8_cvt_pk(f[4], f[5]); w.w = g8_cvt_pk(f[6], f[7]);
;             *(u32x4*)(d + nn * 64 + kc * 8) = w;
;         }
.LBB0_1616:
	s_or_b64 exec, exec, s[4:5]
	s_waitcnt lgkmcnt(0)
	s_barrier
	ds_read_b32 v11, v15
	s_mov_b64 s[4:5], -1
	s_waitcnt lgkmcnt(0)
	v_cmp_lt_i32_e32 vcc, s11, v11
	v_readfirstlane_b32 s0, v11
	s_cbranch_vccnz .LBB0_1611
	s_cmpk_gt_i32 s0, 0xaef
	s_cselect_b64 vcc, -1, 0
	s_and_b64 s[4:5], vcc, exec
	s_cselect_b32 s4, s13, 0x104e000
	s_cselect_b32 s9, 0x400, s12
	s_cselect_b32 s15, s73, s69
	s_cselect_b32 s18, s72, s68
	s_cselect_b32 s5, s14, 0x1510
	s_cselect_b32 s16, 20, 21
	s_cselect_b32 s19, 10, 11
	s_add_u32 s20, s78, s4
	s_addc_u32 s21, s79, 0
	s_lshr_b32 s6, s9, 4
	s_abs_i32 s4, s6
	v_cvt_f32_u32_e32 v11, s4
	s_sub_i32 s17, 0, s4
	s_add_i32 s5, s5, s0
	s_abs_i32 s7, s5
	v_rcp_iflag_f32_e32 v11, v11
	s_xor_b32 s0, s5, s6
	s_lshr_b32 s8, s9, 8
	s_ashr_i32 s0, s0, 31
	v_mul_f32_e32 v11, 0x4f7ffffe, v11
	v_cvt_u32_f32_e32 v11, v11
	s_nop 0
	v_readfirstlane_b32 s22, v11
	s_mul_i32 s17, s17, s22
	s_mul_hi_u32 s17, s22, s17
	s_add_i32 s22, s22, s17
	s_mul_hi_u32 s17, s7, s22
	s_mul_i32 s22, s17, s4
	s_sub_i32 s7, s7, s22
	s_add_i32 s22, s17, 1
	s_sub_i32 s23, s7, s4
	s_cmp_ge_u32 s7, s4
	s_cselect_b32 s17, s22, s17
	s_cselect_b32 s7, s23, s7
	s_add_i32 s22, s17, 1
	s_cmp_ge_u32 s7, s4
	s_cselect_b32 s4, s22, s17
	s_xor_b32 s4, s4, s0
	s_sub_i32 s4, s4, s0
	s_sext_i32_i8 s0, s8
	v_cvt_f32_i32_e32 v11, s0
	s_mul_i32 s6, s4, s6
	s_sub_i32 s5, s5, s6
	v_cvt_f32_i32_e32 v28, s5
	v_rcp_iflag_f32_e32 v29, v11
	s_xor_b32 s0, s5, s0
	s_ashr_i32 s0, s0, 30
	s_or_b32 s0, s0, 1
	v_mul_f32_e32 v29, v28, v29
	v_trunc_f32_e32 v29, v29
	v_fma_f32 v28, -v29, v11, v28
	v_cvt_i32_f32_e32 v29, v29
	v_cmp_ge_f32_e64 s[6:7], |v28|, |v11|
	s_and_b64 s[6:7], s[6:7], exec
	s_cselect_b32 s0, s0, 0
	v_readfirstlane_b32 s6, v29
	s_add_i32 s6, s6, s0
	s_mul_i32 s7, s6, s8
	s_sub_i32 s8, s5, s7
	s_sext_i32_i8 s5, s8
	v_lshl_add_u32 v11, s5, 7, v12
	v_lshl_or_b32 v28, s5, 8, v13
	s_ashr_i32 s5, s4, 31
	s_sext_i32_i8 s0, s6
	s_lshl_b64 s[16:17], s[4:5], s16
	v_lshl_or_b32 v30, s0, 6, v14
	s_lshl_b64 s[16:17], s[16:17], 2
	v_ashrrev_i32_e32 v31, 31, v30
	s_add_u32 s16, s18, s16
	v_cndmask_b32_e32 v28, v11, v28, vcc
	s_addc_u32 s17, s15, s17
	v_lshlrev_b64 v[30:31], s19, v[30:31]
	v_lshl_add_u64 v[30:31], v[30:31], 2, s[16:17]
	v_ashrrev_i32_e32 v29, 31, v28
	v_lshl_add_u64 v[52:53], v[28:29], 2, v[30:31]
	s_lshl_b64 s[16:17], 12, s19
	s_lshl_b32 s0, s9, 2
	v_lshl_add_u64 v[40:41], v[52:53], 0, s[16:17]
	s_lshl_b64 s[16:17], 24, s19
	v_lshl_add_u64 v[36:37], v[52:53], 0, s[0:1]
	v_lshl_add_u64 v[44:45], v[52:53], 0, s[16:17]
	s_lshl_b64 s[16:17], 28, s19
	v_lshl_add_u64 v[54:55], v[36:37], 0, s[0:1]
	v_lshl_add_u64 v[48:49], v[52:53], 0, s[16:17]
	s_lshl_b32 s0, s9, 3
	s_lshl_b64 s[16:17], 20, s19
	global_load_dwordx4 v[28:31], v[52:53], off nt
	global_load_dwordx4 v[32:35], v[36:37], off nt
	s_nop 0
	global_load_dwordx4 v[36:39], v[54:55], off nt
	s_nop 0
	global_load_dwordx4 v[40:43], v[40:41], off nt
	v_lshl_add_u64 v[54:55], v[54:55], 0, s[0:1]
	v_lshl_add_u64 v[56:57], v[52:53], 0, s[16:17]
	global_load_dwordx4 v[44:47], v[44:45], off nt
	s_nop 0
	global_load_dwordx4 v[48:51], v[48:49], off nt
	s_nop 0
	global_load_dwordx4 v[52:55], v[54:55], off nt
	s_nop 0
	global_load_dwordx4 v[56:59], v[56:57], off nt
	s_lshl_b64 s[4:5], s[4:5], s19
	s_lshl_b64 s[4:5], s[4:5], 11
	s_add_u32 s0, s20, s4
	s_addc_u32 s9, s21, s5
	s_bfe_i64 s[4:5], s[8:9], 0x80000
	s_bfe_i64 s[6:7], s[6:7], 0x80000
	s_lshl_b64 s[4:5], s[4:5], 19
	s_add_u32 s0, s0, s4
	s_addc_u32 s8, s9, s5
	s_lshl_b64 s[4:5], s[6:7], 15
	s_add_u32 s4, s0, s4
	s_addc_u32 s5, s8, s5
	v_mov_b32_e32 v11, v3
	s_add_i32 s3, s3, -1
	s_cmp_eq_u32 s3, 0
	s_waitcnt vmcnt(7)
	ds_write_b128 v16, v[28:31]
	s_waitcnt vmcnt(6)
	ds_write2_b32 v17, v32, v33 offset1:1
	ds_write2_b32 v18, v34, v35 offset1:1
	s_waitcnt vmcnt(3)
	ds_write2_b64 v24, v[44:45], v[46:47] offset1:1
	s_waitcnt vmcnt(2)
	ds_write2_b32 v25, v48, v49 offset1:1
	ds_write2_b32 v26, v50, v51 offset1:1
	ds_write2_b64 v19, v[36:37], v[38:39] offset1:1
	ds_write2_b32 v20, v40, v41 offset1:1
	ds_write2_b32 v21, v42, v43 offset1:1
	s_waitcnt vmcnt(1)
	ds_write_b128 v16, v[52:55] offset:4112
	s_waitcnt vmcnt(0)
	ds_write2_b32 v22, v56, v57 offset1:1
	ds_write2_b32 v23, v58, v59 offset1:1
	s_waitcnt lgkmcnt(0)
	s_barrier
	ds_read_b32 v28, v27 offset:1028
	ds_read_b32 v29, v27 offset:3084
	ds_read_b32 v30, v27 offset:5140
	ds_read_b32 v31, v27 offset:7196
	ds_read_b32 v32, v27 offset:6168
	ds_read_b32 v33, v27 offset:4112
	ds_read_b32 v34, v27 offset:2056
	ds_read_b32 v35, v27
	s_waitcnt lgkmcnt(0)
	v_cvt_pk_bf16_f32 v28, v35, v28
	v_cvt_pk_bf16_f32 v29, v34, v29
	v_cvt_pk_bf16_f32 v30, v33, v30
	v_cvt_pk_bf16_f32 v31, v32, v31
	ds_read_b32 v36, v27 offset:1060
	ds_read_b32 v37, v27 offset:3116
	ds_read_b32 v38, v27 offset:5172
	ds_read_b32 v39, v27 offset:7228
	ds_read_b32 v40, v27 offset:6200
	ds_read_b32 v41, v27 offset:4144
	ds_read_b32 v42, v27 offset:2088
	ds_read_b32 v43, v27 offset:32
	v_lshl_add_u64 v[32:33], s[4:5], 0, v[2:3]
	v_lshl_add_u64 v[34:35], v[32:33], 0, v[10:11]
	global_store_dwordx4 v[34:35], v[28:31], off
	v_lshl_add_u64 v[34:35], v[4:5], 1, v[32:33]
	s_cselect_b64 s[4:5], -1, 0
	s_waitcnt lgkmcnt(0)
	v_cvt_pk_bf16_f32 v28, v43, v36
	v_cvt_pk_bf16_f32 v29, v42, v37
	v_cvt_pk_bf16_f32 v30, v41, v38
	v_cvt_pk_bf16_f32 v31, v40, v39
	ds_read_b32 v11, v27 offset:1092
	ds_read_b32 v36, v27 offset:3148
	ds_read_b32 v37, v27 offset:6232
	ds_read_b32 v38, v27 offset:4176
	ds_read_b32 v39, v27 offset:2120
	ds_read_b32 v40, v27 offset:64
	ds_read_b32 v41, v27 offset:5204
	ds_read_b32 v42, v27 offset:7260
	global_store_dwordx4 v[34:35], v[28:31], off
	v_lshl_add_u64 v[34:35], v[6:7], 1, v[32:33]
	v_lshl_add_u64 v[32:33], v[8:9], 1, v[32:33]
	s_waitcnt lgkmcnt(2)
	v_cvt_pk_bf16_f32 v28, v40, v11
	v_cvt_pk_bf16_f32 v29, v39, v36
	s_waitcnt lgkmcnt(1)
	v_cvt_pk_bf16_f32 v30, v38, v41
	s_waitcnt lgkmcnt(0)
	v_cvt_pk_bf16_f32 v31, v37, v42
	ds_read_b32 v11, v27 offset:1124
	ds_read_b32 v36, v27 offset:3180
	ds_read_b32 v37, v27 offset:6264
	ds_read_b32 v38, v27 offset:4208
	ds_read_b32 v39, v27 offset:2152
	ds_read_b32 v40, v27 offset:96
	ds_read_b32 v41, v27 offset:5236
	ds_read_b32 v42, v27 offset:7292
	global_store_dwordx4 v[34:35], v[28:31], off
	s_waitcnt lgkmcnt(2)
	s_nop 0
	v_cvt_pk_bf16_f32 v28, v40, v11
	v_cvt_pk_bf16_f32 v29, v39, v36
	s_waitcnt lgkmcnt(1)
	v_cvt_pk_bf16_f32 v30, v38, v41
	s_waitcnt lgkmcnt(0)
	v_cvt_pk_bf16_f32 v31, v37, v42
	global_store_dwordx4 v[32:33], v[28:31], off
	s_branch .LBB0_1611

; #define LAS __attribute__((address_space(3)))
; #define SEAM(k) do { if (IN(k) && IN((k) + 1)) xcd_barrier(bar); \
;         if (PROBE_MASK) { const unsigned long long t_ = __builtin_amdgcn_s_memrealtime(); if ((PROBE_MASK >> (k)) & 1u) pr_acc += t_ - pr_t0; pr_t0 = t_; } } while (0)
; __device__ __forceinline__ void convert_deferred(const Ptrs& P, unsigned char* lds, int quota) {
;     const int tid = threadIdx.x, wid = tid >> 6, lane = tid & 63;
;     float* tile = (float*)lds;
;     volatile __attribute__((address_space(3))) int* slot = (volatile __attribute__((address_space(3))) int*)((__attribute__((address_space(3))) unsigned char*)lds + 131072 + 320 + 11000);
;     unsigned* q = (unsigned*)(P.ws + WS_CTL) + CW_DEFQ;
;     for (int n = 0; n < quota; ++n) {
;         __syncthreads();
;         if (tid == 0) *slot = (int)atomicAdd(q, 1u);
;         __syncthreads();
;         const int t = *slot;
;         if (t >= DEF_GU + DEF_DN) break;
;         const bool gu = t < DEF_GU;
;         const float* src = gu ? P.in[34] : P.in[36]; bf16* dst = (bf16*)(P.ws + (gu ? WS_WGU : WS_WDN));
;         const int N = gu ? 2048 : 1024, ntn = N / 256, it = gu ? 2 * NE * 16 * 8 - DEF_GU + t : 2 * NE * 16 * 4 - DEF_DN + (t - DEF_GU);
; __global__ void __launch_bounds__(NT, 2) mega(Args args) {
;     ...
;     if (IN(11)) { g8::DenseOrder S; S.init(H, D, (const bf16*)(ws + WS_WODIN), D, R, ODD_IN, G, (int)blockIdx.x, 0);
;         g8::EpiDiffIn E{Z, P.in[25], P.in[26], (const float*)(ws + WS_ROPE), (const float*)(ws + WS_ROPE) + SEQ * 64, (LAS float*)(LDSP + MISC_OFF + 1024)};
;         g8::gemm_phase<g8::EpiDiffIn, g8::DenseOrder, false, true>(LDSP, D, D, S, E);
;         if (IDLE_LAST(68 * 12)) convert_deferred(P, lds, 4); } SEAM(11);
.LBB0_1851:
	s_abs_i32 s0, s62
	v_cvt_f32_u32_e32 v2, s0
	s_sub_i32 s3, 0, s0
	v_readlane_b32 s56, v254, 40
	s_mov_b32 s1, 0
	v_rcp_iflag_f32_e32 v2, v2
	v_readlane_b32 s57, v254, 41
	v_mul_f32_e32 v2, 0x4f7ffffe, v2
	v_cvt_u32_f32_e32 v2, v2
	s_nop 0
	v_readfirstlane_b32 s4, v2
	s_mul_i32 s3, s3, s4
	s_mul_hi_u32 s3, s4, s3
	s_add_i32 s4, s4, s3
	s_mul_hi_u32 s3, s4, 0x330
	s_mul_i32 s3, s3, s0
	s_sub_i32 s3, 0x330, s3
	s_sub_i32 s4, s3, s0
	s_cmp_ge_u32 s3, s0
	s_cselect_b32 s3, s4, s3
	s_sub_i32 s4, s3, s0
	s_cmp_ge_u32 s3, s0
	s_cselect_b32 s0, s4, s3
	s_cmp_eq_u32 s0, 0
	s_cselect_b64 s[4:5], -1, 0
	s_cmp_lt_i32 s2, s0
	s_cselect_b64 s[6:7], -1, 0
	s_or_b64 s[4:5], s[4:5], s[6:7]
	s_and_b64 vcc, exec, s[4:5]
	s_cbranch_vccnz .LBB0_1861
	v_and_b32_e32 v2, 0x7c, v218
	v_lshlrev_b32_e32 v3, 5, v0
	s_movk_i32 s0, 0x400
	v_and_or_b32 v12, v3, s0, v2
	v_bfe_u32 v2, v0, 3, 3
	v_lshl_or_b32 v4, v1, 5, v2
	v_lshlrev_b32_e32 v2, 3, v0
	v_lshl_add_u32 v11, v182, 4, 0
	v_and_b32_e32 v2, 56, v2
	v_mul_u32_u24_e32 v16, 0x2020, v1
	v_mov_b32_e32 v3, 0
	s_waitcnt vmcnt(0)
	v_lshl_add_u32 v27, v4, 2, 0
	v_mul_u32_u24_e32 v28, 0x404, v2
	v_lshlrev_b32_e32 v10, 6, v4
	s_add_i32 s10, 0, 0x22c38
	v_add_u32_e32 v16, v11, v16
	v_and_b32_e32 v13, 0xfc, v218
	v_and_b32_e32 v14, 56, v179
	s_mov_b32 s3, 10
	v_or_b32_e32 v4, 0x200, v10
	v_mov_b32_e32 v5, v3
	v_or_b32_e32 v6, 0x400, v10
	v_mov_b32_e32 v7, v3
	v_or_b32_e32 v8, 0x600, v10
	v_mov_b32_e32 v9, v3
	v_mov_b32_e32 v15, s10
	s_movk_i32 s11, 0xff9
	s_movk_i32 s12, 0x800
	s_mov_b32 s13, 0x1104e000
	s_movk_i32 s14, 0x6
	v_add_u32_e32 v17, 0x404, v16
	v_add_u32_e32 v18, 0x40c, v16
	v_add_u32_e32 v19, 0x808, v16
	v_add_u32_e32 v20, 0xc0c, v16
	v_add_u32_e32 v21, 0xc14, v16
	v_add_u32_e32 v22, 0x1414, v16
	v_add_u32_e32 v23, 0x141c, v16
	v_add_u32_e32 v24, 0x1818, v16
	v_add_u32_e32 v25, 0x1c1c, v16
	v_add_u32_e32 v26, 0x1c24, v16
	v_lshlrev_b32_e32 v2, 1, v2
	v_add_u32_e32 v27, v27, v28
	v_lshlrev_b32_e32 v10, 1, v10
	s_branch .LBB0_1854

; __device__ __forceinline__ unsigned g8_cvt_pk(float lo, float hi) { unsigned r; asm volatile("v_cvt_pk_bf16_f32 %0, %1, %2" : "=v"(r) : "v"(lo), "v"(hi)); return r; }
; __device__ __forceinline__ void convert_deferred(const Ptrs& P, unsigned char* lds, int quota) {
;     ...
;         __syncthreads();
;         if (tid == 0) *slot = (int)atomicAdd(q, 1u);
;         __syncthreads();
;         const int t = *slot;
;         if (t >= DEF_GU + DEF_DN) break;
;         const bool gu = t < DEF_GU;
;         const float* src = gu ? P.in[34] : P.in[36]; bf16* dst = (bf16*)(P.ws + (gu ? WS_WGU : WS_WDN));
;         const int N = gu ? 2048 : 1024, ntn = N / 256, it = gu ? 2 * NE * 16 * 8 - DEF_GU + t : 2 * NE * 16 * 4 - DEF_DN + (t - DEF_GU);
;         f32x4 cur[8];
;         bt_load(src, N, gu ? 1 : 0, it, ntn, cur);
; #pragma unroll
;         for (int i = 0; i < 8; ++i) { float* tp = tile + (wid * 8 + i) * 257 + lane * 4; tp[0] = cur[i][0]; tp[1] = cur[i][1]; tp[2] = cur[i][2]; tp[3] = cur[i][3]; }
;         __syncthreads();
;         const int per = 16 * ntn, z = it / per, r = it % per, kt = r / ntn, nt = r % ntn;
;         bf16* d = dst + (size_t)z * N * 1024 + (((size_t)nt * 16 + kt) << 14);
;         const int kc = lane & 7;
; #pragma unroll
;         for (int pss = 0; pss < 4; ++pss) {
;             const int nn = wid * 32 + pss * 8 + (lane >> 3); float f[8];
; #pragma unroll
;             for (int j = 0; j < 8; ++j) f[j] = tile[(kc * 8 + j) * 257 + nn];
;             u32x4 w; w.x = g8_cvt_pk(f[0], f[1]); w.y = g8_cvt_pk(f[2], f[3]); w.z = g8_cvt_pk(f[4], f[5]); w.w = g8_cvt_pk(f[6], f[7]);
;             *(u32x4*)(d + nn * 64 + kc * 8) = w;
;         }
.LBB0_1858:
	s_or_b64 exec, exec, s[4:5]
	s_waitcnt lgkmcnt(0)
	s_barrier
	ds_read_b32 v11, v15
	s_mov_b64 s[4:5], -1
	s_waitcnt lgkmcnt(0)
	v_cmp_lt_i32_e32 vcc, s11, v11
	v_readfirstlane_b32 s0, v11
	s_cbranch_vccnz .LBB0_1853
	s_cmpk_gt_i32 s0, 0xaef
	s_cselect_b64 vcc, -1, 0
	s_and_b64 s[4:5], vcc, exec
	s_cselect_b32 s4, s13, 0x104e000
	s_cselect_b32 s9, 0x400, s12
	s_cselect_b32 s15, s73, s69
	s_cselect_b32 s20, s72, s68
	s_cselect_b32 s5, s14, 0x1510
	s_cselect_b32 s16, 20, 21
	s_cselect_b32 s21, 10, 11
	s_add_u32 s22, s78, s4
	s_addc_u32 s23, s79, 0
	s_lshr_b32 s6, s9, 4
	s_abs_i32 s4, s6
	v_cvt_f32_u32_e32 v11, s4
	s_sub_i32 s17, 0, s4
	s_add_i32 s5, s5, s0
	s_abs_i32 s7, s5
	v_rcp_iflag_f32_e32 v11, v11
	s_xor_b32 s0, s5, s6
	s_lshr_b32 s8, s9, 8
	s_ashr_i32 s0, s0, 31
	v_mul_f32_e32 v11, 0x4f7ffffe, v11
	v_cvt_u32_f32_e32 v11, v11
	s_nop 0
	v_readfirstlane_b32 s24, v11
	s_mul_i32 s17, s17, s24
	s_mul_hi_u32 s17, s24, s17
	s_add_i32 s24, s24, s17
	s_mul_hi_u32 s17, s7, s24
	s_mul_i32 s24, s17, s4
	s_sub_i32 s7, s7, s24
	s_add_i32 s24, s17, 1
	s_sub_i32 s25, s7, s4
	s_cmp_ge_u32 s7, s4
	s_cselect_b32 s17, s24, s17
	s_cselect_b32 s7, s25, s7
	s_add_i32 s24, s17, 1
	s_cmp_ge_u32 s7, s4
	s_cselect_b32 s4, s24, s17
	s_xor_b32 s4, s4, s0
	s_sub_i32 s4, s4, s0
	s_sext_i32_i8 s0, s8
	v_cvt_f32_i32_e32 v11, s0
	s_mul_i32 s6, s4, s6
	s_sub_i32 s5, s5, s6
	v_cvt_f32_i32_e32 v28, s5
	v_rcp_iflag_f32_e32 v29, v11
	s_xor_b32 s0, s5, s0
	s_ashr_i32 s0, s0, 30
	s_or_b32 s0, s0, 1
	v_mul_f32_e32 v29, v28, v29
	v_trunc_f32_e32 v29, v29
	v_fma_f32 v28, -v29, v11, v28
	v_cvt_i32_f32_e32 v29, v29
	v_cmp_ge_f32_e64 s[6:7], |v28|, |v11|
	s_and_b64 s[6:7], s[6:7], exec
	s_cselect_b32 s0, s0, 0
	v_readfirstlane_b32 s6, v29
	s_add_i32 s6, s6, s0
	s_mul_i32 s7, s6, s8
	s_sub_i32 s8, s5, s7
	s_sext_i32_i8 s5, s8
	v_lshl_add_u32 v11, s5, 7, v12
	v_lshl_or_b32 v28, s5, 8, v13
	s_ashr_i32 s5, s4, 31
	s_sext_i32_i8 s0, s6
	s_lshl_b64 s[16:17], s[4:5], s16
	v_lshl_or_b32 v30, s0, 6, v14
	s_lshl_b64 s[16:17], s[16:17], 2
	v_ashrrev_i32_e32 v31, 31, v30
	s_add_u32 s16, s20, s16
	v_cndmask_b32_e32 v28, v11, v28, vcc
	s_addc_u32 s17, s15, s17
	v_lshlrev_b64 v[30:31], s21, v[30:31]
	v_lshl_add_u64 v[30:31], v[30:31], 2, s[16:17]
	v_ashrrev_i32_e32 v29, 31, v28
	v_lshl_add_u64 v[52:53], v[28:29], 2, v[30:31]
	s_lshl_b64 s[16:17], 12, s21
	s_lshl_b32 s0, s9, 2
	v_lshl_add_u64 v[40:41], v[52:53], 0, s[16:17]
	s_lshl_b64 s[16:17], 24, s21
	v_lshl_add_u64 v[36:37], v[52:53], 0, s[0:1]
	v_lshl_add_u64 v[44:45], v[52:53], 0, s[16:17]
	s_lshl_b64 s[16:17], 28, s21
	v_lshl_add_u64 v[54:55], v[36:37], 0, s[0:1]
	v_lshl_add_u64 v[48:49], v[52:53], 0, s[16:17]
	s_lshl_b32 s0, s9, 3
	s_lshl_b64 s[16:17], 20, s21
	global_load_dwordx4 v[28:31], v[52:53], off nt
	global_load_dwordx4 v[32:35], v[36:37], off nt
	s_nop 0
	global_load_dwordx4 v[36:39], v[54:55], off nt
	s_nop 0
	global_load_dwordx4 v[40:43], v[40:41], off nt
	v_lshl_add_u64 v[54:55], v[54:55], 0, s[0:1]
	v_lshl_add_u64 v[56:57], v[52:53], 0, s[16:17]
	global_load_dwordx4 v[44:47], v[44:45], off nt
	s_nop 0
	global_load_dwordx4 v[48:51], v[48:49], off nt
	s_nop 0
	global_load_dwordx4 v[52:55], v[54:55], off nt
	s_nop 0
	global_load_dwordx4 v[56:59], v[56:57], off nt
	s_lshl_b64 s[4:5], s[4:5], s21
	s_lshl_b64 s[4:5], s[4:5], 11
	s_add_u32 s0, s22, s4
	s_addc_u32 s9, s23, s5
	s_bfe_i64 s[4:5], s[8:9], 0x80000
	s_bfe_i64 s[6:7], s[6:7], 0x80000
	s_lshl_b64 s[4:5], s[4:5], 19
	s_add_u32 s0, s0, s4
	s_addc_u32 s8, s9, s5
	s_lshl_b64 s[4:5], s[6:7], 15
	s_add_u32 s4, s0, s4
	s_addc_u32 s5, s8, s5
	v_mov_b32_e32 v11, v3
	s_add_i32 s3, s3, -1
	s_cmp_eq_u32 s3, 0
	s_waitcnt vmcnt(7)
	ds_write_b128 v16, v[28:31]
	s_waitcnt vmcnt(6)
	ds_write2_b32 v17, v32, v33 offset1:1
	ds_write2_b32 v18, v34, v35 offset1:1
	s_waitcnt vmcnt(3)
	ds_write2_b64 v24, v[44:45], v[46:47] offset1:1
	s_waitcnt vmcnt(2)
	ds_write2_b32 v25, v48, v49 offset1:1
	ds_write2_b32 v26, v50, v51 offset1:1
	ds_write2_b64 v19, v[36:37], v[38:39] offset1:1
	ds_write2_b32 v20, v40, v41 offset1:1
	ds_write2_b32 v21, v42, v43 offset1:1
	s_waitcnt vmcnt(1)
	ds_write_b128 v16, v[52:55] offset:4112
	s_waitcnt vmcnt(0)
	ds_write2_b32 v22, v56, v57 offset1:1
	ds_write2_b32 v23, v58, v59 offset1:1
	s_waitcnt lgkmcnt(0)
	s_barrier
	ds_read_b32 v28, v27 offset:1028
	ds_read_b32 v29, v27 offset:3084
	ds_read_b32 v30, v27 offset:5140
	ds_read_b32 v31, v27 offset:7196
	ds_read_b32 v32, v27 offset:6168
	ds_read_b32 v33, v27 offset:4112
	ds_read_b32 v34, v27 offset:2056
	ds_read_b32 v35, v27
	s_waitcnt lgkmcnt(0)
	v_cvt_pk_bf16_f32 v28, v35, v28
	v_cvt_pk_bf16_f32 v29, v34, v29
	v_cvt_pk_bf16_f32 v30, v33, v30
	v_cvt_pk_bf16_f32 v31, v32, v31
	ds_read_b32 v36, v27 offset:1060
	ds_read_b32 v37, v27 offset:3116
	ds_read_b32 v38, v27 offset:5172
	ds_read_b32 v39, v27 offset:7228
	ds_read_b32 v40, v27 offset:6200
	ds_read_b32 v41, v27 offset:4144
	ds_read_b32 v42, v27 offset:2088
	ds_read_b32 v43, v27 offset:32
	v_lshl_add_u64 v[32:33], s[4:5], 0, v[2:3]
	v_lshl_add_u64 v[34:35], v[32:33], 0, v[10:11]
	global_store_dwordx4 v[34:35], v[28:31], off
	v_lshl_add_u64 v[34:35], v[4:5], 1, v[32:33]
	s_cselect_b64 s[4:5], -1, 0
	s_waitcnt lgkmcnt(0)
	v_cvt_pk_bf16_f32 v28, v43, v36
	v_cvt_pk_bf16_f32 v29, v42, v37
	v_cvt_pk_bf16_f32 v30, v41, v38
	v_cvt_pk_bf16_f32 v31, v40, v39
	ds_read_b32 v11, v27 offset:1092
	ds_read_b32 v36, v27 offset:3148
	ds_read_b32 v37, v27 offset:6232
	ds_read_b32 v38, v27 offset:4176
	ds_read_b32 v39, v27 offset:2120
	ds_read_b32 v40, v27 offset:64
	ds_read_b32 v41, v27 offset:5204
	ds_read_b32 v42, v27 offset:7260
	global_store_dwordx4 v[34:35], v[28:31], off
	v_lshl_add_u64 v[34:35], v[6:7], 1, v[32:33]
	v_lshl_add_u64 v[32:33], v[8:9], 1, v[32:33]
	s_waitcnt lgkmcnt(2)
	v_cvt_pk_bf16_f32 v28, v40, v11
	v_cvt_pk_bf16_f32 v29, v39, v36
	s_waitcnt lgkmcnt(1)
	v_cvt_pk_bf16_f32 v30, v38, v41
	s_waitcnt lgkmcnt(0)
	v_cvt_pk_bf16_f32 v31, v37, v42
	ds_read_b32 v11, v27 offset:1124
	ds_read_b32 v36, v27 offset:3180
	ds_read_b32 v37, v27 offset:6264
	ds_read_b32 v38, v27 offset:4208
	ds_read_b32 v39, v27 offset:2152
	ds_read_b32 v40, v27 offset:96
	ds_read_b32 v41, v27 offset:5236
	ds_read_b32 v42, v27 offset:7292
	global_store_dwordx4 v[34:35], v[28:31], off
	s_waitcnt lgkmcnt(2)
	s_nop 0
	v_cvt_pk_bf16_f32 v28, v40, v11
	v_cvt_pk_bf16_f32 v29, v39, v36
	s_waitcnt lgkmcnt(1)
	v_cvt_pk_bf16_f32 v30, v38, v41
	s_waitcnt lgkmcnt(0)
	v_cvt_pk_bf16_f32 v31, v37, v42
	global_store_dwordx4 v[32:33], v[28:31], off
	s_branch .LBB0_1853

; #define SEAM(k) do { if (IN(k) && IN((k) + 1)) xcd_barrier(bar); \
;         if (PROBE_MASK) { const unsigned long long t_ = __builtin_amdgcn_s_memrealtime(); if ((PROBE_MASK >> (k)) & 1u) pr_acc += t_ - pr_t0; pr_t0 = t_; } } while (0)
; __device__ __forceinline__ void convert_deferred(const Ptrs& P, unsigned char* lds, int quota) {
;     const int tid = threadIdx.x, wid = tid >> 6, lane = tid & 63;
;     float* tile = (float*)lds;
;     volatile __attribute__((address_space(3))) int* slot = (volatile __attribute__((address_space(3))) int*)((__attribute__((address_space(3))) unsigned char*)lds + 131072 + 320 + 11000);
;     unsigned* q = (unsigned*)(P.ws + WS_CTL) + CW_DEFQ;
;     for (int n = 0; n < quota; ++n) {
;         __syncthreads();
;         if (tid == 0) *slot = (int)atomicAdd(q, 1u);
;         __syncthreads();
;         const int t = *slot;
;         if (t >= DEF_GU + DEF_DN) break;
;         const bool gu = t < DEF_GU;
;         const float* src = gu ? P.in[34] : P.in[36]; bf16* dst = (bf16*)(P.ws + (gu ? WS_WGU : WS_WDN));
;         const int N = gu ? 2048 : 1024, ntn = N / 256, it = gu ? 2 * NE * 16 * 8 - DEF_GU + t : 2 * NE * 16 * 4 - DEF_DN + (t - DEF_GU);
; __global__ void __launch_bounds__(NT, 2) mega(Args args) {
;     ...
;     if (IN(15)) { ph_norm2_router(P, lds, 1, 1); convert_deferred(P, lds, 1 << 20); } SEAM(15);
.LBB0_2278:
	v_and_b32_e32 v2, 0x7c, v179
	v_lshlrev_b32_e32 v3, 5, v0
	s_movk_i32 s0, 0x400
	v_and_or_b32 v12, v3, s0, v2
	v_lshrrev_b32_e32 v2, 3, v0
	v_and_b32_e32 v14, 56, v2
	v_lshrrev_b32_e32 v2, 3, v182
	v_lshl_or_b32 v4, v1, 5, v2
	v_lshl_add_u32 v5, v182, 4, 0
	v_and_b32_e32 v2, 56, v188
	v_lshl_add_u32 v7, v4, 2, 0
	v_mul_u32_u24_e32 v11, 0x2020, v1
	v_lshlrev_b32_e32 v4, 6, v4
	v_mul_u32_u24_e32 v9, 0x404, v2
	v_or_b32_e32 v6, 0x200, v4
	v_or_b32_e32 v8, 0x400, v4
	v_or_b32_e32 v10, 0x600, v4
	s_add_i32 s10, 0, 0x22c38
	v_add_u32_e32 v16, v5, v11
	v_and_b32_e32 v13, 0xfc, v179
	s_mov_b32 s1, 0
	v_mov_b32_e32 v3, 0
	s_mov_b32 s3, 0x100000
	v_mov_b32_e32 v15, s10
	s_movk_i32 s11, 0xff9
	s_movk_i32 s12, 0x800
	s_mov_b32 s13, 0x1104e000
	s_movk_i32 s14, 0x6
	v_add_u32_e32 v17, 0x404, v16
	v_add_u32_e32 v18, 0x40c, v16
	v_add_u32_e32 v19, 0x808, v16
	v_add_u32_e32 v20, 0xc0c, v16
	v_add_u32_e32 v21, 0xc14, v16
	v_add_u32_e32 v22, 0x1414, v16
	v_add_u32_e32 v23, 0x141c, v16
	v_add_u32_e32 v24, 0x1818, v16
	v_add_u32_e32 v25, 0x1c1c, v16
	v_add_u32_e32 v26, 0x1c24, v16
	v_lshlrev_b32_e32 v2, 1, v2
	v_add_u32_e32 v27, v7, v9
	v_lshlrev_b32_e32 v4, 1, v4
	v_lshlrev_b32_e32 v6, 1, v6
	v_lshlrev_b32_e32 v8, 1, v8
	v_lshlrev_b32_e32 v10, 1, v10
	s_branch .LBB0_2280

; __device__ __forceinline__ unsigned g8_cvt_pk(float lo, float hi) { unsigned r; asm volatile("v_cvt_pk_bf16_f32 %0, %1, %2" : "=v"(r) : "v"(lo), "v"(hi)); return r; }
; __device__ __forceinline__ void convert_deferred(const Ptrs& P, unsigned char* lds, int quota) {
;     ...
;         __syncthreads();
;         if (tid == 0) *slot = (int)atomicAdd(q, 1u);
;         __syncthreads();
;         const int t = *slot;
;         if (t >= DEF_GU + DEF_DN) break;
;         const bool gu = t < DEF_GU;
;         const float* src = gu ? P.in[34] : P.in[36]; bf16* dst = (bf16*)(P.ws + (gu ? WS_WGU : WS_WDN));
;         const int N = gu ? 2048 : 1024, ntn = N / 256, it = gu ? 2 * NE * 16 * 8 - DEF_GU + t : 2 * NE * 16 * 4 - DEF_DN + (t - DEF_GU);
;         f32x4 cur[8];
;         bt_load(src, N, gu ? 1 : 0, it, ntn, cur);
; #pragma unroll
;         for (int i = 0; i < 8; ++i) { float* tp = tile + (wid * 8 + i) * 257 + lane * 4; tp[0] = cur[i][0]; tp[1] = cur[i][1]; tp[2] = cur[i][2]; tp[3] = cur[i][3]; }
;         __syncthreads();
;         const int per = 16 * ntn, z = it / per, r = it % per, kt = r / ntn, nt = r % ntn;
;         bf16* d = dst + (size_t)z * N * 1024 + (((size_t)nt * 16 + kt) << 14);
;         const int kc = lane & 7;
; #pragma unroll
;         for (int pss = 0; pss < 4; ++pss) {
;             const int nn = wid * 32 + pss * 8 + (lane >> 3); float f[8];
; #pragma unroll
;             for (int j = 0; j < 8; ++j) f[j] = tile[(kc * 8 + j) * 257 + nn];
;             u32x4 w; w.x = g8_cvt_pk(f[0], f[1]); w.y = g8_cvt_pk(f[2], f[3]); w.z = g8_cvt_pk(f[4], f[5]); w.w = g8_cvt_pk(f[6], f[7]);
;             *(u32x4*)(d + nn * 64 + kc * 8) = w;
;         }
.LBB0_2284:
	s_or_b64 exec, exec, s[4:5]
	s_waitcnt lgkmcnt(0)
	s_barrier
	ds_read_b32 v5, v15
	s_mov_b64 s[4:5], -1
	s_waitcnt lgkmcnt(0)
	v_cmp_lt_i32_e32 vcc, s11, v5
	v_readfirstlane_b32 s0, v5
	s_cbranch_vccnz .LBB0_2279
	s_cmpk_gt_i32 s0, 0xaef
	s_cselect_b64 vcc, -1, 0
	s_and_b64 s[4:5], vcc, exec
	s_cselect_b32 s4, s13, 0x104e000
	s_cselect_b32 s9, 0x400, s12
	s_cselect_b32 s15, s73, s69
	s_cselect_b32 s18, s72, s68
	s_cselect_b32 s5, s14, 0x1510
	s_cselect_b32 s16, 20, 21
	s_cselect_b32 s19, 10, 11
	s_add_u32 s22, s78, s4
	s_addc_u32 s23, s79, 0
	s_lshr_b32 s6, s9, 4
	s_abs_i32 s4, s6
	v_cvt_f32_u32_e32 v5, s4
	s_sub_i32 s17, 0, s4
	s_add_i32 s5, s5, s0
	s_abs_i32 s7, s5
	v_rcp_iflag_f32_e32 v5, v5
	s_xor_b32 s0, s5, s6
	s_lshr_b32 s8, s9, 8
	s_ashr_i32 s0, s0, 31
	v_mul_f32_e32 v5, 0x4f7ffffe, v5
	v_cvt_u32_f32_e32 v5, v5
	s_nop 0
	v_readfirstlane_b32 s24, v5
	s_mul_i32 s17, s17, s24
	s_mul_hi_u32 s17, s24, s17
	s_add_i32 s24, s24, s17
	s_mul_hi_u32 s17, s7, s24
	s_mul_i32 s24, s17, s4
	s_sub_i32 s7, s7, s24
	s_add_i32 s24, s17, 1
	s_sub_i32 s25, s7, s4
	s_cmp_ge_u32 s7, s4
	s_cselect_b32 s17, s24, s17
	s_cselect_b32 s7, s25, s7
	s_add_i32 s24, s17, 1
	s_cmp_ge_u32 s7, s4
	s_cselect_b32 s4, s24, s17
	s_xor_b32 s4, s4, s0
	s_sub_i32 s4, s4, s0
	s_sext_i32_i8 s0, s8
	v_cvt_f32_i32_e32 v5, s0
	s_mul_i32 s6, s4, s6
	s_sub_i32 s5, s5, s6
	v_cvt_f32_i32_e32 v7, s5
	v_rcp_iflag_f32_e32 v9, v5
	s_xor_b32 s0, s5, s0
	s_ashr_i32 s0, s0, 30
	s_or_b32 s0, s0, 1
	v_mul_f32_e32 v9, v7, v9
	v_trunc_f32_e32 v9, v9
	v_fma_f32 v7, -v9, v5, v7
	v_cvt_i32_f32_e32 v9, v9
	v_cmp_ge_f32_e64 s[6:7], |v7|, |v5|
	s_and_b64 s[6:7], s[6:7], exec
	s_cselect_b32 s0, s0, 0
	v_readfirstlane_b32 s6, v9
	s_add_i32 s6, s6, s0
	s_mul_i32 s7, s6, s8
	s_sub_i32 s8, s5, s7
	s_sext_i32_i8 s5, s8
	v_lshl_add_u32 v5, s5, 7, v12
	v_lshl_or_b32 v7, s5, 8, v13
	s_ashr_i32 s5, s4, 31
	s_sext_i32_i8 s0, s6
	s_lshl_b64 s[16:17], s[4:5], s16
	v_lshl_or_b32 v30, s0, 6, v14
	s_lshl_b64 s[16:17], s[16:17], 2
	v_ashrrev_i32_e32 v31, 31, v30
	s_add_u32 s16, s18, s16
	v_cndmask_b32_e32 v28, v5, v7, vcc
	s_addc_u32 s17, s15, s17
	v_lshlrev_b64 v[30:31], s19, v[30:31]
	v_lshl_add_u64 v[30:31], v[30:31], 2, s[16:17]
	v_ashrrev_i32_e32 v29, 31, v28
	v_lshl_add_u64 v[52:53], v[28:29], 2, v[30:31]
	s_lshl_b32 s0, s9, 2
	s_lshl_b64 s[16:17], 12, s19
	v_lshl_add_u64 v[36:37], v[52:53], 0, s[0:1]
	v_lshl_add_u64 v[44:45], v[52:53], 0, s[16:17]
	s_lshl_b64 s[16:17], 24, s19
	v_lshl_add_u64 v[54:55], v[36:37], 0, s[0:1]
	v_lshl_add_u64 v[56:57], v[52:53], 0, s[16:17]
	s_lshl_b64 s[16:17], 28, s19
	s_lshl_b32 s0, s9, 3
	v_lshl_add_u64 v[58:59], v[52:53], 0, s[16:17]
	v_lshl_add_u64 v[60:61], v[54:55], 0, s[0:1]
	s_lshl_b64 s[16:17], 20, s19
	global_load_dwordx4 v[28:31], v[52:53], off nt
	global_load_dwordx4 v[32:35], v[36:37], off nt
	s_nop 0
	global_load_dwordx4 v[36:39], v[54:55], off nt
	global_load_dwordx4 v[40:43], v[44:45], off nt
	s_nop 0
	global_load_dwordx4 v[44:47], v[56:57], off nt
	global_load_dwordx4 v[48:51], v[58:59], off nt
	v_lshl_add_u64 v[62:63], v[52:53], 0, s[16:17]
	global_load_dwordx4 v[52:55], v[60:61], off nt
	global_load_dwordx4 v[56:59], v[62:63], off nt
	s_lshl_b64 s[4:5], s[4:5], s19
	s_lshl_b64 s[4:5], s[4:5], 11
	s_add_u32 s0, s22, s4
	s_addc_u32 s9, s23, s5
	s_bfe_i64 s[4:5], s[8:9], 0x80000
	s_bfe_i64 s[6:7], s[6:7], 0x80000
	s_lshl_b64 s[4:5], s[4:5], 19
	s_add_u32 s0, s0, s4
	s_addc_u32 s8, s9, s5
	s_lshl_b64 s[4:5], s[6:7], 15
	s_add_u32 s4, s0, s4
	s_addc_u32 s5, s8, s5
	v_mov_b32_e32 v5, v3
	s_add_i32 s3, s3, -1
	s_cmp_eq_u32 s3, 0
	s_waitcnt vmcnt(7)
	ds_write_b128 v16, v[28:31]
	s_waitcnt vmcnt(6)
	ds_write2_b32 v17, v32, v33 offset1:1
	ds_write2_b32 v18, v34, v35 offset1:1
	s_waitcnt vmcnt(3)
	ds_write2_b64 v24, v[44:45], v[46:47] offset1:1
	s_waitcnt vmcnt(2)
	ds_write2_b32 v25, v48, v49 offset1:1
	ds_write2_b32 v26, v50, v51 offset1:1
	ds_write2_b64 v19, v[36:37], v[38:39] offset1:1
	ds_write2_b32 v20, v40, v41 offset1:1
	ds_write2_b32 v21, v42, v43 offset1:1
	s_waitcnt vmcnt(1)
	ds_write_b128 v16, v[52:55] offset:4112
	s_waitcnt vmcnt(0)
	ds_write2_b32 v22, v56, v57 offset1:1
	ds_write2_b32 v23, v58, v59 offset1:1
	s_waitcnt lgkmcnt(0)
	s_barrier
	ds_read_b32 v7, v27 offset:1028
	ds_read_b32 v9, v27 offset:3084
	ds_read_b32 v11, v27 offset:5140
	ds_read_b32 v31, v27 offset:7196
	ds_read_b32 v32, v27 offset:6168
	ds_read_b32 v30, v27 offset:4112
	ds_read_b32 v29, v27 offset:2056
	ds_read_b32 v28, v27
	s_waitcnt lgkmcnt(0)
	v_cvt_pk_bf16_f32 v28, v28, v7
	v_cvt_pk_bf16_f32 v29, v29, v9
	v_cvt_pk_bf16_f32 v30, v30, v11
	v_cvt_pk_bf16_f32 v31, v32, v31
	ds_read_b32 v7, v27 offset:1060
	ds_read_b32 v9, v27 offset:3116
	ds_read_b32 v11, v27 offset:5172
	ds_read_b32 v36, v27 offset:7228
	ds_read_b32 v37, v27 offset:6200
	ds_read_b32 v38, v27 offset:4144
	ds_read_b32 v39, v27 offset:2088
	ds_read_b32 v40, v27 offset:32
	v_lshl_add_u64 v[32:33], s[4:5], 0, v[2:3]
	v_lshl_add_u64 v[34:35], v[32:33], 0, v[4:5]
	global_store_dwordx4 v[34:35], v[28:31], off
	s_cselect_b64 s[4:5], -1, 0
	s_waitcnt lgkmcnt(0)
	v_cvt_pk_bf16_f32 v28, v40, v7
	v_cvt_pk_bf16_f32 v29, v39, v9
	v_cvt_pk_bf16_f32 v30, v38, v11
	v_cvt_pk_bf16_f32 v31, v37, v36
	ds_read_b32 v5, v27 offset:1092
	ds_read_b32 v9, v27 offset:3148
	ds_read_b32 v11, v27 offset:5204
	ds_read_b32 v36, v27 offset:6232
	ds_read_b32 v37, v27 offset:4176
	ds_read_b32 v38, v27 offset:2120
	ds_read_b32 v39, v27 offset:64
	ds_read_b32 v40, v27 offset:7260
	v_mov_b32_e32 v7, v3
	v_lshl_add_u64 v[34:35], v[32:33], 0, v[6:7]
	global_store_dwordx4 v[34:35], v[28:31], off
	s_waitcnt lgkmcnt(1)
	s_nop 0
	v_cvt_pk_bf16_f32 v28, v39, v5
	v_cvt_pk_bf16_f32 v29, v38, v9
	v_cvt_pk_bf16_f32 v30, v37, v11
	s_waitcnt lgkmcnt(0)
	v_cvt_pk_bf16_f32 v31, v36, v40
	ds_read_b32 v5, v27 offset:1124
	ds_read_b32 v7, v27 offset:3180
	ds_read_b32 v11, v27 offset:5236
	ds_read_b32 v36, v27 offset:6264
	ds_read_b32 v37, v27 offset:4208
	ds_read_b32 v38, v27 offset:2152
	ds_read_b32 v39, v27 offset:96
	ds_read_b32 v40, v27 offset:7292
	v_mov_b32_e32 v9, v3
	v_lshl_add_u64 v[34:35], v[32:33], 0, v[8:9]
	global_store_dwordx4 v[34:35], v[28:31], off
	s_waitcnt lgkmcnt(1)
	s_nop 0
	v_cvt_pk_bf16_f32 v28, v39, v5
	v_cvt_pk_bf16_f32 v29, v38, v7
	v_cvt_pk_bf16_f32 v30, v37, v11
	v_mov_b32_e32 v11, v3
	v_lshl_add_u64 v[32:33], v[32:33], 0, v[10:11]
	s_waitcnt lgkmcnt(0)
	v_cvt_pk_bf16_f32 v31, v36, v40
	global_store_dwordx4 v[32:33], v[28:31], off
	s_branch .LBB0_2279
